# L1 mixer int8 quantise item loops software-pipelined: next item's address math + 17 loads issued into holding registers before the current item is converted; T1 row loop counted vmcnt
# baseline (speedup 1.0000x reference)
; __device__ __forceinline__ unsigned pack_i8x4(float a, float b, float c, float d) {
;     const int ia = (int)rintf(fminf(fmaxf(a, -127.f), 127.f)), ib = (int)rintf(fminf(fmaxf(b, -127.f), 127.f)), ic = (int)rintf(fminf(fmaxf(c, -127.f), 127.f)), id = (int)rintf(fminf(fmaxf(d, -127.f), 127.f));
;     return (unsigned)(ia & 0xff) | ((unsigned)(ib & 0xff) << 8) | ((unsigned)(ic & 0xff) << 16) | ((unsigned)(id & 0xff) << 24);
; template <int YMODE, int EXTRA, bool NORM_OUT, bool XN8  , bool XIN_BF = false  , bool XOUT_BF = false  > ...
;     ...
;                     const float inv = am > 0.f ? 127.f / am : 0.f;
;                     if (F.lane == 0) { rowmax[row] = am; if (EXTRA == 2) route[384 + rl] = am; }
; #pragma unroll
;                     for (int j = 0; j < 8; ++j) *(unsigned*)((unsigned char*)XN + row * D + 256 * j + 4 * F.lane) = pack_i8x4(x[j][0] * inv, x[j][1] * inv, x[j][2] * inv, x[j][3] * inv);
.LBB0_1084:
	s_or_b64 exec, exec, s[8:9]
	v_div_scale_f32 v104, s[8:9], s14, s14, v125
	v_rcp_f32_e32 v105, v104
	v_mov_b32_e32 v106, s14
	v_div_scale_f32 v106, vcc, s21, v106, s21
	v_fma_f32 v107, -v104, v105, 1.0
	v_fmac_f32_e32 v105, v107, v105
	v_mul_f32_e32 v107, v106, v105
	v_fma_f32 v108, -v104, v107, v106
	v_fmac_f32_e32 v107, v108, v105
	v_fma_f32 v104, -v104, v107, v106
	v_div_fmas_f32 v104, v104, v105, v107
	v_div_fixup_f32 v104, v104, s14, v125
	v_cmp_gt_f32_e64 vcc, s14, 0
	s_lshl_b64 s[8:9], s[16:17], 11
	s_add_i32 s24, s24, 1
	v_cndmask_b32_e32 v104, 0, v104, vcc
	v_mul_f32_e32 v65, v65, v104
	v_mul_f32_e32 v61, v61, v104
	v_mul_f32_e32 v57, v57, v104
	v_mul_f32_e32 v53, v53, v104
	v_mul_f32_e32 v49, v49, v104
	v_mul_f32_e32 v45, v45, v104
	v_mul_f32_e32 v41, v41, v104
	v_mul_f32_e32 v37, v37, v104
	v_mul_f32_e32 v64, v64, v104
	v_mul_f32_e32 v62, v62, v104
	v_mul_f32_e32 v63, v63, v104
	v_med3_f32 v65, v65, s22, v125
	v_mul_f32_e32 v60, v60, v104
	v_mul_f32_e32 v58, v58, v104
	v_mul_f32_e32 v59, v59, v104
	v_med3_f32 v61, v61, s22, v125
	v_mul_f32_e32 v56, v56, v104
	v_mul_f32_e32 v54, v54, v104
	v_mul_f32_e32 v55, v55, v104
	v_med3_f32 v57, v57, s22, v125
	v_mul_f32_e32 v52, v52, v104
	v_mul_f32_e32 v50, v50, v104
	v_mul_f32_e32 v51, v51, v104
	v_med3_f32 v53, v53, s22, v125
	v_mul_f32_e32 v48, v48, v104
	v_mul_f32_e32 v46, v46, v104
	v_mul_f32_e32 v47, v47, v104
	v_med3_f32 v49, v49, s22, v125
	v_mul_f32_e32 v44, v44, v104
	v_mul_f32_e32 v42, v42, v104
	v_mul_f32_e32 v43, v43, v104
	v_med3_f32 v45, v45, s22, v125
	v_mul_f32_e32 v40, v40, v104
	v_mul_f32_e32 v38, v38, v104
	v_mul_f32_e32 v39, v39, v104
	v_med3_f32 v41, v41, s22, v125
	v_mul_f32_e32 v36, v36, v104
	v_mul_f32_e32 v34, v34, v104
	v_mul_f32_e32 v35, v35, v104
	v_med3_f32 v37, v37, s22, v125
	v_med3_f32 v64, v64, s22, v125
	v_rndne_f32_e32 v65, v65
	v_med3_f32 v62, v62, s22, v125
	v_med3_f32 v63, v63, s22, v125
	v_med3_f32 v60, v60, s22, v125
	v_rndne_f32_e32 v61, v61
	v_med3_f32 v58, v58, s22, v125
	v_med3_f32 v59, v59, s22, v125
	v_med3_f32 v56, v56, s22, v125
	v_rndne_f32_e32 v57, v57
	v_med3_f32 v54, v54, s22, v125
	v_med3_f32 v55, v55, s22, v125
	v_med3_f32 v52, v52, s22, v125
	v_rndne_f32_e32 v53, v53
	v_med3_f32 v50, v50, s22, v125
	v_med3_f32 v51, v51, s22, v125
	v_med3_f32 v48, v48, s22, v125
	v_rndne_f32_e32 v49, v49
	v_med3_f32 v46, v46, s22, v125
	v_med3_f32 v47, v47, s22, v125
	v_med3_f32 v44, v44, s22, v125
	v_rndne_f32_e32 v45, v45
	v_med3_f32 v42, v42, s22, v125
	v_med3_f32 v43, v43, s22, v125
	v_med3_f32 v40, v40, s22, v125
	v_rndne_f32_e32 v41, v41
	v_med3_f32 v38, v38, s22, v125
	v_med3_f32 v39, v39, s22, v125
	v_med3_f32 v36, v36, s22, v125
	v_rndne_f32_e32 v37, v37
	v_med3_f32 v34, v34, s22, v125
	v_med3_f32 v35, v35, s22, v125
	v_rndne_f32_e32 v64, v64
	v_cvt_i32_f32_e32 v65, v65
	v_rndne_f32_e32 v62, v62
	v_rndne_f32_e32 v63, v63
	v_rndne_f32_e32 v60, v60
	v_cvt_i32_f32_e32 v61, v61
	v_rndne_f32_e32 v58, v58
	v_rndne_f32_e32 v59, v59
	v_rndne_f32_e32 v56, v56
	v_cvt_i32_f32_e32 v57, v57
	v_rndne_f32_e32 v54, v54
	v_rndne_f32_e32 v55, v55
	v_rndne_f32_e32 v52, v52
	v_cvt_i32_f32_e32 v53, v53
	v_rndne_f32_e32 v50, v50
	v_rndne_f32_e32 v51, v51
	v_rndne_f32_e32 v48, v48
	v_cvt_i32_f32_e32 v49, v49
	v_rndne_f32_e32 v46, v46
	v_rndne_f32_e32 v47, v47
	v_rndne_f32_e32 v44, v44
	v_cvt_i32_f32_e32 v45, v45
	v_rndne_f32_e32 v42, v42
	v_rndne_f32_e32 v43, v43
	v_rndne_f32_e32 v40, v40
	v_cvt_i32_f32_e32 v41, v41
	v_rndne_f32_e32 v38, v38
	v_rndne_f32_e32 v39, v39
	v_rndne_f32_e32 v36, v36
	v_cvt_i32_f32_e32 v37, v37
	v_rndne_f32_e32 v34, v34
	v_rndne_f32_e32 v35, v35
	v_cvt_i32_f32_e32 v64, v64
	v_cvt_i32_f32_sdwa v62, v62 dst_sel:WORD_1 dst_unused:UNUSED_PAD src0_sel:DWORD
	v_cvt_i32_f32_e32 v63, v63
	v_cvt_i32_f32_e32 v60, v60
	v_cvt_i32_f32_sdwa v58, v58 dst_sel:WORD_1 dst_unused:UNUSED_PAD src0_sel:DWORD
	v_cvt_i32_f32_e32 v59, v59
	v_cvt_i32_f32_e32 v56, v56
	v_cvt_i32_f32_sdwa v54, v54 dst_sel:WORD_1 dst_unused:UNUSED_PAD src0_sel:DWORD
	v_cvt_i32_f32_e32 v55, v55
	v_cvt_i32_f32_e32 v52, v52
	v_cvt_i32_f32_sdwa v50, v50 dst_sel:WORD_1 dst_unused:UNUSED_PAD src0_sel:DWORD
	v_cvt_i32_f32_e32 v51, v51
	v_cvt_i32_f32_e32 v48, v48
	v_cvt_i32_f32_sdwa v46, v46 dst_sel:WORD_1 dst_unused:UNUSED_PAD src0_sel:DWORD
	v_cvt_i32_f32_e32 v47, v47
	v_cvt_i32_f32_e32 v44, v44
	v_cvt_i32_f32_sdwa v42, v42 dst_sel:WORD_1 dst_unused:UNUSED_PAD src0_sel:DWORD
	v_cvt_i32_f32_e32 v43, v43
	v_cvt_i32_f32_e32 v40, v40
	v_cvt_i32_f32_sdwa v38, v38 dst_sel:WORD_1 dst_unused:UNUSED_PAD src0_sel:DWORD
	v_cvt_i32_f32_e32 v39, v39
	v_cvt_i32_f32_e32 v36, v36
	v_cvt_i32_f32_sdwa v34, v34 dst_sel:WORD_1 dst_unused:UNUSED_PAD src0_sel:DWORD
	v_cvt_i32_f32_e32 v35, v35
	v_lshlrev_b32_e32 v65, 8, v65
	v_lshlrev_b32_e32 v61, 8, v61
	v_lshlrev_b32_e32 v57, 8, v57
	v_lshlrev_b32_e32 v53, 8, v53
	v_lshlrev_b32_e32 v49, 8, v49
	v_lshlrev_b32_e32 v45, 8, v45
	v_lshlrev_b32_e32 v41, 8, v41
	v_lshlrev_b32_e32 v37, 8, v37
	v_and_b32_e32 v65, 0xff00, v65
	v_and_b32_e32 v62, 0xff0000, v62
	v_perm_b32 v63, v63, v64, s23
	v_and_b32_e32 v61, 0xff00, v61
	v_and_b32_e32 v58, 0xff0000, v58
	v_perm_b32 v59, v59, v60, s23
	v_and_b32_e32 v57, 0xff00, v57
	v_and_b32_e32 v54, 0xff0000, v54
	v_perm_b32 v55, v55, v56, s23
	v_and_b32_e32 v53, 0xff00, v53
	v_and_b32_e32 v50, 0xff0000, v50
	v_perm_b32 v51, v51, v52, s23
	v_and_b32_e32 v49, 0xff00, v49
	v_and_b32_e32 v46, 0xff0000, v46
	v_perm_b32 v47, v47, v48, s23
	v_and_b32_e32 v45, 0xff00, v45
	v_and_b32_e32 v42, 0xff0000, v42
	v_perm_b32 v43, v43, v44, s23
	v_and_b32_e32 v41, 0xff00, v41
	v_and_b32_e32 v38, 0xff0000, v38
	v_perm_b32 v39, v39, v40, s23
	v_and_b32_e32 v37, 0xff00, v37
	v_and_b32_e32 v34, 0xff0000, v34
	v_perm_b32 v35, v35, v36, s23
	v_or3_b32 v64, v63, v65, v62
	v_lshl_add_u64 v[62:63], v[86:87], 0, s[8:9]
	v_or3_b32 v58, v59, v61, v58
	v_or3_b32 v54, v55, v57, v54
	v_or3_b32 v50, v51, v53, v50
	v_or3_b32 v46, v47, v49, v46
	v_or3_b32 v42, v43, v45, v42
	v_or3_b32 v38, v39, v41, v38
	v_or3_b32 v34, v35, v37, v34
	global_store_dword v[62:63], v64, off
	global_store_dword v[62:63], v58, off offset:256
	global_store_dword v[62:63], v54, off offset:512
	global_store_dword v[62:63], v50, off offset:768
	global_store_dword v[62:63], v46, off offset:1024
	global_store_dword v[62:63], v42, off offset:1280
	global_store_dword v[62:63], v38, off offset:1536
	global_store_dword v[62:63], v34, off offset:1792
	s_waitcnt vmcnt(17)
; __device__ __forceinline__ float bflo(unsigned u) { return __uint_as_float(u << 16); }
; __device__ __forceinline__ float bfhi(unsigned u) { return __uint_as_float(u & 0xffff0000u); }
; template <int YMODE, int EXTRA, bool NORM_OUT, bool XN8  , bool XIN_BF = false  , bool XOUT_BF = false  > ...
;     ...
;         RP_LOAD(0);
; #pragma unroll 1
;         for (int rr = 0; rr < 8; ++rr) {
;             const int rl = F.wave * 8 + ((rr + blk) & 7); const size_t row = (size_t)blk * 64 + rl;
;             asm volatile("" ::: "memory");
;             f32x4 x[8];
; #pragma unroll
;             for (int j = 0; j < 8; ++j) x[j] = XIN_BF ? (f32x4){bflo(xrb[j].x), bfhi(xrb[j].x), bflo(xrb[j].y), bfhi(xrb[j].y)} : xr[j];
;             f32x4 y[8];
;             if (YMODE == 1) {
; #pragma unroll
;                 for (int j = 0; j < 8; ++j) y[j] = (f32x4){bflo(yr[j].x), bfhi(yr[j].x), bflo(yr[j].y), bfhi(yr[j].y)};
;             }
;             if (YMODE == 2) {
; #pragma unroll
;                 for (int j = 0; j < 8; ++j) y[j] = (f32x4){bflo(yr[j].x), bfhi(yr[j].x), bflo(yr[j].y), bfhi(yr[j].y)} * w1n + (f32x4){bflo(yr2[j].x), bfhi(yr2[j].x), bflo(yr2[j].y), bfhi(yr2[j].y)} * w2n;
;             }
;             if (rr < 7) RP_LOAD(rr + 1);
	v_mov_b64_e32 v[64:65], v[4:5]
	v_mov_b64_e32 v[60:61], v[8:9]
	v_mov_b64_e32 v[56:57], v[12:13]
	v_mov_b64_e32 v[52:53], v[16:17]
	v_mov_b64_e32 v[48:49], v[20:21]
	v_mov_b64_e32 v[44:45], v[24:25]
	v_mov_b64_e32 v[40:41], v[28:29]
	v_mov_b64_e32 v[36:37], v[32:33]
	s_cmp_eq_u32 s24, 8
	v_mov_b64_e32 v[104:105], v[88:89]
	v_mov_b64_e32 v[106:107], v[90:91]
	v_mov_b64_e32 v[108:109], v[92:93]
	v_mov_b64_e32 v[110:111], v[94:95]
	v_mov_b64_e32 v[112:113], v[96:97]
	v_mov_b64_e32 v[114:115], v[98:99]
	v_mov_b64_e32 v[116:117], v[100:101]
	v_mov_b64_e32 v[118:119], v[102:103]
	v_mov_b64_e32 v[62:63], v[2:3]
	v_mov_b64_e32 v[58:59], v[6:7]
	v_mov_b64_e32 v[54:55], v[10:11]
	v_mov_b64_e32 v[50:51], v[14:15]
	v_mov_b64_e32 v[46:47], v[18:19]
	v_mov_b64_e32 v[42:43], v[22:23]
	v_mov_b64_e32 v[38:39], v[26:27]
	v_mov_b64_e32 v[34:35], v[30:31]
	s_cbranch_scc1 .LBB0_1082

; __device__ __forceinline__ void cvt_item_i8(const float* src, int ld, int k0, int c0, unsigned char* dst, int Kd, int drow0, const float* cmx  , unsigned char* scr, int lane) {
;     const int c = lane & 7, q = lane >> 3;
;     const f32x4 cm = *(const f32x4*)(cmx + 4 * c);
;     f32x4 inv; inv[0] = cm[0] > 0.f ? 127.f / cm[0] : 0.f; inv[1] = cm[1] > 0.f ? 127.f / cm[1] : 0.f; inv[2] = cm[2] > 0.f ? 127.f / cm[2] : 0.f; inv[3] = cm[3] > 0.f ? 127.f / cm[3] : 0.f;
;     f32x4 v[4][4];
; #pragma unroll
;     for (int g = 0; g < 4; ++g)
; #pragma unroll
;         for (int j = 0; j < 4; ++j) v[g][j] = __builtin_nontemporal_load((const f32x4*)(src + (size_t)(k0 + 32 * g + 4 * q + j) * ld + c0 + 4 * c));
; template <int GRP>
; __device__ __forceinline__ void conv_item(Frame& F, int r) {
;     ...
;     else { constexpr int KBN = (GRP == 3) ? 16 : CMS_KB, I_E = KBN * 88; const int up = r / (8 * I_E); r %= (8 * I_E); const int e = r / I_E; r %= I_E; const int kb = r / 88, nb = r % 88, n0 = nb * 32, drow = (n0 >> 7) * 256 + up * 128 + (n0 & 127);
;         if (GRP == 3) cvt_item_i8(inptr(F, up ? IN_MU : IN_MG) + (size_t)e * D * DFE, DFE, kb * 128, n0, ws + WS_MGU + (size_t)e * 2 * DFE * D, D, drow, cmx + 2 * DFF + e * 2 * DFE + drow, scr, F.lane);
;     ...
;     for (int it = first + F.gw; it < N; it += F.NGW) conv_item<GRP>(F, it);
.LBB0_1672:
	s_mul_hi_i32 s0, s3, 0x2e8ba2e9
	s_lshr_b32 s1, s0, 31
	s_ashr_i32 s0, s0, 11
	s_add_i32 s0, s0, s1
	s_mul_i32 s1, s0, 0xffffd400
	s_lshl_b32 s6, s0, 7
	s_add_i32 s0, s3, s1
	s_mul_i32 s1, s0, 0xba3
	s_lshr_b32 s7, s1, 31
	s_ashr_i32 s1, s1, 22
	s_add_i32 s1, s1, s7
	s_mul_i32 s7, s1, 0x580
	s_sub_i32 s0, s0, s7
	s_sext_i32_i16 s36, s0
	s_mulk_i32 s36, 0xba3
	s_lshr_b32 s38, s36, 31
	s_ashr_i32 s36, s36, 18
	s_add_i32 s38, s36, s38
	s_sext_i32_i16 s36, s38
	s_mulk_i32 s38, 0x58
	s_sub_i32 s0, s0, s38
	s_sext_i32_i16 s38, s0
	s_lshl_b32 s0, s38, 5
	s_lshl_b32 s38, s38, 6
	s_and_b32 s38, s38, 0xffffff00
	s_and_b32 s39, s0, 0x60
	s_add_i32 s38, s38, s6
	s_add_i32 s37, s3, 0x2bff
	s_or_b32 s6, s38, s39
	s_cmpk_lt_u32 s37, 0x57ff
	s_cselect_b32 s37, s15, 0xa8
	v_or_b32_e32 v8, s6, v17
	s_add_i32 s37, s37, 0
	v_ashrrev_i32_e32 v9, 31, v8
	s_add_i32 s37, s37, 0x20200
	v_lshlrev_b64 v[98:99], 11, v[8:9]
	v_mov_b32_e32 v8, s37
	ds_read_b64 v[8:9], v8
	s_sext_i32_i16 s11, s1
	s_mul_i32 s9, s11, 0x1600000
	s_mul_hi_i32 s1, s11, 0x1600000
	s_mul_i32 s10, s11, 0xb00000
	s_waitcnt lgkmcnt(0)
	v_readfirstlane_b32 s37, v8
	v_readfirstlane_b32 s38, v9
	s_add_u32 s9, s37, s9
	s_addc_u32 s37, s38, s1
	s_lshl_b32 s36, s36, 7
	s_mul_hi_i32 s7, s11, 0xb00000
	s_add_u32 s10, s4, s10
	s_mul_hi_i32 s8, s11, 0x5800
	s_mulk_i32 s11, 0x5800
	s_addc_u32 s38, s12, s7
	s_add_u32 s1, s13, s11
	s_addc_u32 s8, s14, s8
	s_ashr_i32 s7, s6, 31
	v_or_b32_e32 v6, s6, v1
	v_or_b32_e32 v10, s6, v18
	v_or_b32_e32 v12, s6, v19
	s_lshl_b64 s[6:7], s[6:7], 2
	s_add_u32 s6, s1, s6
	s_addc_u32 s7, s8, s7
	s_ashr_i32 s1, s0, 31
	s_lshl_b64 s[0:1], s[0:1], 2
	v_or_b32_e32 v8, s36, v16
	s_add_u32 s0, s9, s0
	v_ashrrev_i32_e32 v11, 31, v10
	v_mul_i32_i24_e32 v8, 0x2c00, v8
	s_addc_u32 s1, s37, s1
	v_lshlrev_b64 v[100:101], 11, v[10:11]
	v_ashrrev_i32_e32 v9, 31, v8
	v_lshl_add_u64 v[10:11], s[0:1], 0, v[4:5]
	v_ashrrev_i32_e32 v7, 31, v6
	v_ashrrev_i32_e32 v13, 31, v12
	v_lshl_add_u64 v[10:11], v[10:11], 0, v[8:9]
	v_lshlrev_b64 v[14:15], 11, v[6:7]
	v_lshlrev_b64 v[6:7], 11, v[12:13]
	v_add_co_u32_e32 v12, vcc, s17, v10
	global_load_dwordx4 v[30:33], v4, s[6:7]
	s_nop 0
	v_addc_co_u32_e32 v13, vcc, 0, v11, vcc
	v_add_co_u32_e32 v42, vcc, s18, v10
	s_ashr_i32 s6, s36, 31
	s_nop 0
	v_addc_co_u32_e32 v43, vcc, 0, v11, vcc
	v_add_co_u32_e32 v46, vcc, s19, v10
	s_add_u32 s0, s10, s36
	s_nop 0
	v_addc_co_u32_e32 v47, vcc, 0, v11, vcc
	v_add_co_u32_e32 v50, vcc, s20, v10
	s_addc_u32 s1, s38, s6
	s_nop 0
	v_addc_co_u32_e32 v51, vcc, 0, v11, vcc
	v_add_co_u32_e32 v54, vcc, s21, v10
	v_lshl_add_u64 v[8:9], s[0:1], 0, v[2:3]
	s_nop 0
	v_addc_co_u32_e32 v55, vcc, 0, v11, vcc
	v_add_co_u32_e32 v58, vcc, s22, v10
	v_lshl_add_u64 v[6:7], v[8:9], 0, v[6:7]
	s_nop 0
	v_addc_co_u32_e32 v59, vcc, 0, v11, vcc
	v_add_co_u32_e32 v62, vcc, s23, v10
	s_add_i32 s3, s3, s40
	s_nop 0
	v_addc_co_u32_e32 v63, vcc, 0, v11, vcc
	v_add_co_u32_e32 v66, vcc, s24, v10
	s_cmpk_lt_i32 s3, 0x5800
	s_nop 0
	v_addc_co_u32_e32 v67, vcc, 0, v11, vcc
	v_add_co_u32_e32 v70, vcc, s25, v10
	s_nop 0
	s_nop 0
	v_addc_co_u32_e32 v71, vcc, 0, v11, vcc
	v_add_co_u32_e32 v74, vcc, s26, v10
	s_nop 0
	s_nop 0
	v_addc_co_u32_e32 v75, vcc, 0, v11, vcc
	v_add_co_u32_e32 v78, vcc, s27, v10
	s_nop 0
	s_nop 0
	v_addc_co_u32_e32 v79, vcc, 0, v11, vcc
	v_add_co_u32_e32 v82, vcc, s28, v10
	s_nop 0
	s_nop 0
	v_addc_co_u32_e32 v83, vcc, 0, v11, vcc
	v_add_co_u32_e32 v86, vcc, s29, v10
	s_nop 0
	s_nop 0
	v_addc_co_u32_e32 v87, vcc, 0, v11, vcc
	v_add_co_u32_e32 v90, vcc, s30, v10
	s_nop 0
	s_nop 0
	v_addc_co_u32_e32 v91, vcc, 0, v11, vcc
	v_add_co_u32_e32 v94, vcc, s31, v10
	s_nop 0
	s_nop 0
	v_addc_co_u32_e32 v95, vcc, 0, v11, vcc
	global_load_dwordx4 v[34:37], v[10:11], off nt
	global_load_dwordx4 v[38:41], v[12:13], off offset:3072 nt
	s_nop 0
	global_load_dwordx4 v[42:45], v[42:43], off offset:2048 nt
	s_nop 0
	global_load_dwordx4 v[46:49], v[46:47], off offset:1024 nt
	s_nop 0
	global_load_dwordx4 v[50:53], v[50:51], off nt
	s_nop 0
	global_load_dwordx4 v[54:57], v[54:55], off offset:3072 nt
	s_nop 0
	global_load_dwordx4 v[58:61], v[58:59], off offset:2048 nt
	s_nop 0
	global_load_dwordx4 v[62:65], v[62:63], off offset:1024 nt
	s_nop 0
	global_load_dwordx4 v[66:69], v[66:67], off nt
	s_nop 0
	global_load_dwordx4 v[70:73], v[70:71], off offset:3072 nt
	s_nop 0
	global_load_dwordx4 v[74:77], v[74:75], off offset:2048 nt
	s_nop 0
	global_load_dwordx4 v[78:81], v[78:79], off offset:1024 nt
	s_nop 0
	global_load_dwordx4 v[82:85], v[82:83], off nt
	s_nop 0
	global_load_dwordx4 v[86:89], v[86:87], off offset:3072 nt
	s_nop 0
	global_load_dwordx4 v[90:93], v[90:91], off offset:2048 nt
	s_nop 0
	global_load_dwordx4 v[94:97], v[94:95], off offset:1024 nt
	s_cselect_b32 s100, 1, 0
	v_lshl_add_u64 v[12:13], v[8:9], 0, v[98:99]
	v_lshl_add_u64 v[10:11], v[8:9], 0, v[14:15]
	v_lshl_add_u64 v[14:15], v[8:9], 0, v[100:101]
	s_waitcnt vmcnt(0)
; __device__ __forceinline__ void cvt_item_i8(const float* src, int ld, int k0, int c0, unsigned char* dst, int Kd, int drow0, const float* cmx  , unsigned char* scr, int lane) {
;     const int c = lane & 7, q = lane >> 3;
;     const f32x4 cm = *(const f32x4*)(cmx + 4 * c);
;     f32x4 inv; inv[0] = cm[0] > 0.f ? 127.f / cm[0] : 0.f; inv[1] = cm[1] > 0.f ? 127.f / cm[1] : 0.f; inv[2] = cm[2] > 0.f ? 127.f / cm[2] : 0.f; inv[3] = cm[3] > 0.f ? 127.f / cm[3] : 0.f;
;     f32x4 v[4][4];
; #pragma unroll
;     for (int g = 0; g < 4; ++g)
; #pragma unroll
;         for (int j = 0; j < 4; ++j) v[g][j] = __builtin_nontemporal_load((const f32x4*)(src + (size_t)(k0 + 32 * g + 4 * q + j) * ld + c0 + 4 * c));
; template <int GRP>
; __device__ __forceinline__ void conv_item(Frame& F, int r) {
;     ...
;     else { constexpr int KBN = (GRP == 3) ? 16 : CMS_KB, I_E = KBN * 88; const int up = r / (8 * I_E); r %= (8 * I_E); const int e = r / I_E; r %= I_E; const int kb = r / 88, nb = r % 88, n0 = nb * 32, drow = (n0 >> 7) * 256 + up * 128 + (n0 & 127);
;         if (GRP == 3) cvt_item_i8(inptr(F, up ? IN_MU : IN_MG) + (size_t)e * D * DFE, DFE, kb * 128, n0, ws + WS_MGU + (size_t)e * 2 * DFE * D, D, drow, cmx + 2 * DFF + e * 2 * DFE + drow, scr, F.lane);
;     ...
;     for (int it = first + F.gw; it < N; it += F.NGW) conv_item<GRP>(F, it);
.Lcv1_R:
	s_bitcmp0_b32 s100, 0
	s_cbranch_scc1 .Lcv1_noP
	s_mul_hi_i32 s0, s3, 0x2e8ba2e9
	s_lshr_b32 s1, s0, 31
	s_ashr_i32 s0, s0, 11
	s_add_i32 s0, s0, s1
	s_mul_i32 s1, s0, 0xffffd400
	s_lshl_b32 s6, s0, 7
	s_add_i32 s0, s3, s1
	s_mul_i32 s1, s0, 0xba3
	s_lshr_b32 s7, s1, 31
	s_ashr_i32 s1, s1, 22
	s_add_i32 s1, s1, s7
	s_mul_i32 s7, s1, 0x580
	s_sub_i32 s0, s0, s7
	s_sext_i32_i16 s36, s0
	s_mulk_i32 s36, 0xba3
	s_lshr_b32 s38, s36, 31
	s_ashr_i32 s36, s36, 18
	s_add_i32 s38, s36, s38
	s_sext_i32_i16 s36, s38
	s_mulk_i32 s38, 0x58
	s_sub_i32 s0, s0, s38
	s_sext_i32_i16 s38, s0
	s_lshl_b32 s0, s38, 5
	s_lshl_b32 s38, s38, 6
	s_and_b32 s38, s38, 0xffffff00
	s_and_b32 s39, s0, 0x60
	s_add_i32 s38, s38, s6
	s_add_i32 s37, s3, 0x2bff
	s_or_b32 s6, s38, s39
	s_cmpk_lt_u32 s37, 0x57ff
	s_cselect_b32 s37, s15, 0xa8
	v_or_b32_e32 v130, s6, v17
	s_add_i32 s37, s37, 0
	v_ashrrev_i32_e32 v131, 31, v130
	s_add_i32 s37, s37, 0x20200
	v_lshlrev_b64 v[124:125], 11, v[130:131]
	v_mov_b32_e32 v130, s37
	ds_read_b64 v[130:131], v130
	s_sext_i32_i16 s11, s1
	s_mul_i32 s9, s11, 0x1600000
	s_mul_hi_i32 s1, s11, 0x1600000
	s_mul_i32 s10, s11, 0xb00000
	s_waitcnt lgkmcnt(0)
	v_readfirstlane_b32 s37, v130
	v_readfirstlane_b32 s38, v131
	s_add_u32 s9, s37, s9
	s_addc_u32 s37, s38, s1
	s_lshl_b32 s36, s36, 7
	s_mul_hi_i32 s7, s11, 0xb00000
	s_add_u32 s10, s4, s10
	s_mul_hi_i32 s8, s11, 0x5800
	s_mulk_i32 s11, 0x5800
	s_addc_u32 s38, s12, s7
	s_add_u32 s1, s13, s11
	s_addc_u32 s8, s14, s8
	s_ashr_i32 s7, s6, 31
	v_or_b32_e32 v128, s6, v1
	v_or_b32_e32 v132, s6, v18
	v_or_b32_e32 v134, s6, v19
	s_lshl_b64 s[6:7], s[6:7], 2
	s_add_u32 s6, s1, s6
	s_addc_u32 s7, s8, s7
	s_ashr_i32 s1, s0, 31
	s_lshl_b64 s[0:1], s[0:1], 2
	v_or_b32_e32 v130, s36, v16
	s_add_u32 s0, s9, s0
	v_ashrrev_i32_e32 v133, 31, v132
	v_mul_i32_i24_e32 v130, 0x2c00, v130
	s_addc_u32 s1, s37, s1
	v_lshlrev_b64 v[126:127], 11, v[132:133]
	v_ashrrev_i32_e32 v131, 31, v130
	v_lshl_add_u64 v[132:133], s[0:1], 0, v[4:5]
	v_ashrrev_i32_e32 v129, 31, v128
	v_ashrrev_i32_e32 v135, 31, v134
	v_lshl_add_u64 v[132:133], v[132:133], 0, v[130:131]
	v_lshlrev_b64 v[136:137], 11, v[128:129]
	v_lshlrev_b64 v[128:129], 11, v[134:135]
	v_add_co_u32_e32 v134, vcc, s17, v132
	global_load_dwordx4 v[120:123], v4, s[6:7]
	s_nop 0
	v_addc_co_u32_e32 v135, vcc, 0, v133, vcc
	v_add_co_u32_e32 v152, vcc, s18, v132
	s_ashr_i32 s6, s36, 31
	s_nop 0
	v_addc_co_u32_e32 v153, vcc, 0, v133, vcc
	v_add_co_u32_e32 v156, vcc, s19, v132
	s_add_u32 s0, s10, s36
	s_nop 0
	v_addc_co_u32_e32 v157, vcc, 0, v133, vcc
	v_add_co_u32_e32 v160, vcc, s20, v132
	s_addc_u32 s1, s38, s6
	s_nop 0
	v_addc_co_u32_e32 v161, vcc, 0, v133, vcc
	v_add_co_u32_e32 v164, vcc, s21, v132
	v_lshl_add_u64 v[130:131], s[0:1], 0, v[2:3]
	s_nop 0
	v_addc_co_u32_e32 v165, vcc, 0, v133, vcc
	v_add_co_u32_e32 v168, vcc, s22, v132
	v_lshl_add_u64 v[128:129], v[130:131], 0, v[128:129]
	s_nop 0
	v_addc_co_u32_e32 v169, vcc, 0, v133, vcc
	v_add_co_u32_e32 v172, vcc, s23, v132
	s_add_i32 s3, s3, s40
	s_nop 0
	v_addc_co_u32_e32 v173, vcc, 0, v133, vcc
	v_add_co_u32_e32 v176, vcc, s24, v132
	s_cmpk_lt_i32 s3, 0x5800
	s_nop 0
	v_addc_co_u32_e32 v177, vcc, 0, v133, vcc
	v_add_co_u32_e32 v180, vcc, s25, v132
	s_nop 0
	s_nop 0
	v_addc_co_u32_e32 v181, vcc, 0, v133, vcc
	v_add_co_u32_e32 v184, vcc, s26, v132
	s_nop 0
	s_nop 0
	v_addc_co_u32_e32 v185, vcc, 0, v133, vcc
	v_add_co_u32_e32 v188, vcc, s27, v132
	s_nop 0
	s_nop 0
	v_addc_co_u32_e32 v189, vcc, 0, v133, vcc
	v_add_co_u32_e32 v210, vcc, s28, v132
	s_nop 0
	s_nop 0
	v_addc_co_u32_e32 v211, vcc, 0, v133, vcc
	v_add_co_u32_e32 v214, vcc, s29, v132
	s_nop 0
	s_nop 0
	v_addc_co_u32_e32 v215, vcc, 0, v133, vcc
	v_add_co_u32_e32 v218, vcc, s30, v132
	s_nop 0
	s_nop 0
	v_addc_co_u32_e32 v219, vcc, 0, v133, vcc
	v_add_co_u32_e32 v222, vcc, s31, v132
	s_nop 0
	s_nop 0
	v_addc_co_u32_e32 v223, vcc, 0, v133, vcc
	global_load_dwordx4 v[144:147], v[132:133], off nt
	global_load_dwordx4 v[148:151], v[134:135], off offset:3072 nt
	s_nop 0
	global_load_dwordx4 v[152:155], v[152:153], off offset:2048 nt
	s_nop 0
	global_load_dwordx4 v[156:159], v[156:157], off offset:1024 nt
	s_nop 0
	global_load_dwordx4 v[160:163], v[160:161], off nt
	s_nop 0
	global_load_dwordx4 v[164:167], v[164:165], off offset:3072 nt
	s_nop 0
	global_load_dwordx4 v[168:171], v[168:169], off offset:2048 nt
	s_nop 0
	global_load_dwordx4 v[172:175], v[172:173], off offset:1024 nt
	s_nop 0
	global_load_dwordx4 v[176:179], v[176:177], off nt
	s_nop 0
	global_load_dwordx4 v[180:183], v[180:181], off offset:3072 nt
	s_nop 0
	global_load_dwordx4 v[184:187], v[184:185], off offset:2048 nt
	s_nop 0
	global_load_dwordx4 v[188:191], v[188:189], off offset:1024 nt
	s_nop 0
	global_load_dwordx4 v[210:213], v[210:211], off nt
	s_nop 0
	global_load_dwordx4 v[214:217], v[214:215], off offset:3072 nt
	s_nop 0
	global_load_dwordx4 v[218:221], v[218:219], off offset:2048 nt
	s_nop 0
	global_load_dwordx4 v[222:225], v[222:223], off offset:1024 nt
	v_lshl_add_u64 v[134:135], v[130:131], 0, v[124:125]
	v_lshl_add_u64 v[132:133], v[130:131], 0, v[136:137]
	v_lshl_add_u64 v[136:137], v[130:131], 0, v[126:127]
	s_cselect_b32 s0, 2, 0
	s_or_b32 s100, s100, s0
; __device__ __forceinline__ unsigned pack_i8x4(float a, float b, float c, float d) {
;     const int ia = (int)rintf(fminf(fmaxf(a, -127.f), 127.f)), ib = (int)rintf(fminf(fmaxf(b, -127.f), 127.f)), ic = (int)rintf(fminf(fmaxf(c, -127.f), 127.f)), id = (int)rintf(fminf(fmaxf(d, -127.f), 127.f));
;     return (unsigned)(ia & 0xff) | ((unsigned)(ib & 0xff) << 8) | ((unsigned)(ic & 0xff) << 16) | ((unsigned)(id & 0xff) << 24);
; __device__ __forceinline__ void cvt_item_i8(const float* src, int ld, int k0, int c0, unsigned char* dst, int Kd, int drow0, const float* cmx  , unsigned char* scr, int lane) {
;     ...
;     f32x4 inv; inv[0] = cm[0] > 0.f ? 127.f / cm[0] : 0.f; inv[1] = cm[1] > 0.f ? 127.f / cm[1] : 0.f; inv[2] = cm[2] > 0.f ? 127.f / cm[2] : 0.f; inv[3] = cm[3] > 0.f ? 127.f / cm[3] : 0.f;
;     f32x4 v[4][4];
; #pragma unroll
;     for (int g = 0; g < 4; ++g)
; #pragma unroll
;         for (int j = 0; j < 4; ++j) v[g][j] = __builtin_nontemporal_load((const f32x4*)(src + (size_t)(k0 + 32 * g + 4 * q + j) * ld + c0 + 4 * c));
; #pragma unroll
;     for (int g = 0; g < 4; ++g)
; #pragma unroll
;         for (int i = 0; i < 4; ++i) *(unsigned*)(scr + (4 * c + i) * 132 + 32 * g + 4 * q) = pack_i8x4(v[g][0][i] * inv[i], v[g][1][i] * inv[i], v[g][2][i] * inv[i], v[g][3][i] * inv[i]);
.Lcv1_noP:
	v_div_scale_f32 v29, s[0:1], v30, v30, s16
	v_rcp_f32_e32 v105, v29
	v_div_scale_f32 v103, s[0:1], v33, v33, s16
	v_fma_f32 v109, -v29, v105, 1.0
	v_rcp_f32_e32 v108, v103
	v_fmac_f32_e32 v105, v109, v105
	v_div_scale_f32 v102, s[8:9], s16, v32, s16
	v_div_scale_f32 v99, s[0:1], v31, v31, s16
	v_rcp_f32_e32 v106, v99
	v_div_scale_f32 v101, s[0:1], v32, v32, s16
	v_rcp_f32_e32 v107, v101
	v_div_scale_f32 v98, vcc, s16, v30, s16
	v_fma_f32 v110, -v99, v106, 1.0
	v_div_scale_f32 v100, s[6:7], s16, v31, s16
	v_fmac_f32_e32 v106, v110, v106
	v_mul_f32_e32 v109, v98, v105
	v_fma_f32 v111, -v101, v107, 1.0
	v_mul_f32_e32 v110, v100, v106
	v_fma_f32 v113, -v29, v109, v98
	v_fmac_f32_e32 v107, v111, v107
	v_fma_f32 v114, -v99, v110, v100
	v_fmac_f32_e32 v109, v113, v105
	v_fma_f32 v112, -v103, v108, 1.0
	v_mul_f32_e32 v111, v102, v107
	v_fmac_f32_e32 v110, v114, v106
	v_fma_f32 v29, -v29, v109, v98
	v_div_scale_f32 v104, s[10:11], s16, v33, s16
	v_fmac_f32_e32 v108, v112, v108
	v_fma_f32 v115, -v101, v111, v102
	v_fma_f32 v98, -v99, v110, v100
	v_div_fmas_f32 v29, v29, v105, v109
	s_mov_b64 vcc, s[6:7]
	v_mul_f32_e32 v112, v104, v108
	v_fmac_f32_e32 v111, v115, v107
	v_div_fixup_f32 v29, v29, v30, s16
	v_div_fmas_f32 v98, v98, v106, v110
	v_cmp_lt_f32_e32 vcc, 0, v30
	v_fma_f32 v116, -v103, v112, v104
	v_fma_f32 v99, -v101, v111, v102
	v_cndmask_b32_e32 v29, 0, v29, vcc
	s_mov_b64 vcc, s[8:9]
	v_fmac_f32_e32 v112, v116, v108
	v_div_fixup_f32 v30, v98, v31, s16
	v_div_fmas_f32 v98, v99, v107, v111
	v_cmp_lt_f32_e32 vcc, 0, v31
	v_fma_f32 v100, -v103, v112, v104
	v_div_fixup_f32 v31, v98, v32, s16
	v_cndmask_b32_e32 v30, 0, v30, vcc
	s_mov_b64 vcc, s[10:11]
	v_div_fmas_f32 v98, v100, v108, v112
	v_cmp_lt_f32_e32 vcc, 0, v32
	v_div_fixup_f32 v32, v98, v33, s16
	s_waitcnt lgkmcnt(0)
	v_mul_f32_e32 v34, v34, v29
	v_mul_f32_e32 v38, v29, v38
	v_mul_f32_e32 v42, v29, v42
	v_mul_f32_e32 v46, v29, v46
	v_mul_f32_e32 v50, v29, v50
	v_mul_f32_e32 v54, v29, v54
	v_mul_f32_e32 v58, v29, v58
	v_mul_f32_e32 v62, v29, v62
	v_mul_f32_e32 v66, v29, v66
	v_mul_f32_e32 v70, v29, v70
	v_mul_f32_e32 v74, v29, v74
	v_mul_f32_e32 v78, v29, v78
	v_mul_f32_e32 v82, v29, v82
	v_mul_f32_e32 v86, v29, v86
	v_cndmask_b32_e32 v31, 0, v31, vcc
	v_med3_f32 v34, v34, s34, v20
	v_med3_f32 v38, v38, s34, v20
	v_med3_f32 v42, v42, s34, v20
	v_med3_f32 v46, v46, s34, v20
	v_mul_f32_e32 v39, v30, v39
	v_mul_f32_e32 v43, v30, v43
	v_mul_f32_e32 v47, v30, v47
	v_med3_f32 v50, v50, s34, v20
	v_med3_f32 v54, v54, s34, v20
	v_mul_f32_e32 v55, v30, v55
	v_cmp_lt_f32_e32 vcc, 0, v33
	v_mul_f32_e32 v90, v29, v90
	v_mul_f32_e32 v35, v35, v30
	v_med3_f32 v58, v58, s34, v20
	v_med3_f32 v62, v62, s34, v20
	v_mul_f32_e32 v51, v30, v51
	v_mul_f32_e32 v59, v30, v59
	v_mul_f32_e32 v63, v30, v63
	v_med3_f32 v66, v66, s34, v20
	v_med3_f32 v70, v70, s34, v20
	v_med3_f32 v74, v74, s34, v20
	v_med3_f32 v78, v78, s34, v20
	v_mul_f32_e32 v71, v30, v71
	v_mul_f32_e32 v79, v30, v79
	v_med3_f32 v82, v82, s34, v20
	v_med3_f32 v86, v86, s34, v20
	v_mul_f32_e32 v87, v30, v87
	v_cndmask_b32_e32 v32, 0, v32, vcc
	v_rndne_f32_e32 v33, v34
	v_rndne_f32_e32 v34, v38
	v_rndne_f32_e32 v38, v42
	v_rndne_f32_e32 v42, v46
	v_med3_f32 v39, v39, s34, v20
	v_med3_f32 v43, v43, s34, v20
	v_med3_f32 v46, v47, s34, v20
	v_mul_f32_e32 v40, v31, v40
	v_mul_f32_e32 v47, v31, v48
	v_rndne_f32_e32 v48, v50
	v_rndne_f32_e32 v50, v54
	v_med3_f32 v55, v55, s34, v20
	v_mul_f32_e32 v56, v31, v56
	v_mul_f32_e32 v29, v29, v94
	v_mul_f32_e32 v67, v30, v67
	v_mul_f32_e32 v75, v30, v75
	v_med3_f32 v90, v90, s34, v20
	v_mul_f32_e32 v83, v30, v83
	v_mul_f32_e32 v91, v30, v91
	v_med3_f32 v35, v35, s34, v20
	v_mul_f32_e32 v36, v36, v31
	v_mul_f32_e32 v44, v31, v44
	v_rndne_f32_e32 v54, v58
	v_rndne_f32_e32 v58, v62
	v_med3_f32 v51, v51, s34, v20
	v_med3_f32 v59, v59, s34, v20
	v_med3_f32 v62, v63, s34, v20
	v_mul_f32_e32 v52, v31, v52
	v_mul_f32_e32 v60, v31, v60
	v_mul_f32_e32 v63, v31, v64
	v_rndne_f32_e32 v64, v66
	v_rndne_f32_e32 v66, v70
	v_rndne_f32_e32 v70, v74
	v_rndne_f32_e32 v74, v78
	v_med3_f32 v71, v71, s34, v20
	v_med3_f32 v78, v79, s34, v20
	v_mul_f32_e32 v72, v31, v72
	v_mul_f32_e32 v79, v31, v80
	v_rndne_f32_e32 v80, v82
	v_rndne_f32_e32 v82, v86
	v_med3_f32 v87, v87, s34, v20
	v_mul_f32_e32 v88, v31, v88
	v_cvt_i32_f32_e32 v34, v34
	v_rndne_f32_e32 v39, v39
	v_rndne_f32_e32 v43, v43
	v_med3_f32 v40, v40, s34, v20
	v_mul_f32_e32 v41, v32, v41
	v_cvt_i32_f32_e32 v50, v50
	v_rndne_f32_e32 v55, v55
	v_med3_f32 v56, v56, s34, v20
	v_mul_f32_e32 v57, v32, v57
	v_med3_f32 v29, v29, s34, v20
	v_mul_f32_e32 v30, v30, v95
	v_med3_f32 v67, v67, s34, v20
	v_med3_f32 v75, v75, s34, v20
	v_mul_f32_e32 v68, v31, v68
	v_mul_f32_e32 v76, v31, v76
	v_rndne_f32_e32 v86, v90
	v_med3_f32 v83, v83, s34, v20
	v_med3_f32 v90, v91, s34, v20
	v_mul_f32_e32 v84, v31, v84
	v_mul_f32_e32 v91, v31, v92
	v_cvt_i32_f32_e32 v33, v33
	v_cvt_i32_f32_sdwa v38, v38 dst_sel:WORD_1 dst_unused:UNUSED_PAD src0_sel:DWORD
	v_rndne_f32_e32 v35, v35
	v_med3_f32 v36, v36, s34, v20
	v_med3_f32 v44, v44, s34, v20
	v_mul_f32_e32 v37, v37, v32
	v_mul_f32_e32 v45, v32, v45
	v_cvt_i32_f32_e32 v48, v48
	v_cvt_i32_f32_sdwa v54, v54 dst_sel:WORD_1 dst_unused:UNUSED_PAD src0_sel:DWORD
	v_rndne_f32_e32 v51, v51
	v_rndne_f32_e32 v59, v59
	v_med3_f32 v52, v52, s34, v20
	v_med3_f32 v60, v60, s34, v20
	v_mul_f32_e32 v53, v32, v53
	v_mul_f32_e32 v61, v32, v61
	v_cvt_i32_f32_e32 v66, v66
	v_rndne_f32_e32 v71, v71
	v_med3_f32 v72, v72, s34, v20
	v_mul_f32_e32 v73, v32, v73
	v_cvt_i32_f32_e32 v82, v82
	v_rndne_f32_e32 v87, v87
	v_med3_f32 v88, v88, s34, v20
	v_mul_f32_e32 v89, v32, v89
; __device__ __forceinline__ unsigned pack_i8x4(float a, float b, float c, float d) {
;     const int ia = (int)rintf(fminf(fmaxf(a, -127.f), 127.f)), ib = (int)rintf(fminf(fmaxf(b, -127.f), 127.f)), ic = (int)rintf(fminf(fmaxf(c, -127.f), 127.f)), id = (int)rintf(fminf(fmaxf(d, -127.f), 127.f));
;     return (unsigned)(ia & 0xff) | ((unsigned)(ib & 0xff) << 8) | ((unsigned)(ic & 0xff) << 16) | ((unsigned)(id & 0xff) << 24);
; __device__ __forceinline__ void cvt_item_i8(const float* src, int ld, int k0, int c0, unsigned char* dst, int Kd, int drow0, const float* cmx  , unsigned char* scr, int lane) {
;     ...
; #pragma unroll
;     for (int g = 0; g < 4; ++g)
; #pragma unroll
;         for (int i = 0; i < 4; ++i) *(unsigned*)(scr + (4 * c + i) * 132 + 32 * g + 4 * q) = pack_i8x4(v[g][0][i] * inv[i], v[g][1][i] * inv[i], v[g][2][i] * inv[i], v[g][3][i] * inv[i]);
	v_cvt_i32_f32_e32 v39, v39
	v_cvt_i32_f32_sdwa v43, v43 dst_sel:WORD_1 dst_unused:UNUSED_PAD src0_sel:DWORD
	v_rndne_f32_e32 v40, v40
	v_med3_f32 v41, v41, s34, v20
	v_cvt_i32_f32_e32 v55, v55
	v_rndne_f32_e32 v56, v56
	v_med3_f32 v57, v57, s34, v20
	v_rndne_f32_e32 v29, v29
	v_med3_f32 v30, v30, s34, v20
	v_mul_f32_e32 v31, v31, v96
	v_cvt_i32_f32_sdwa v42, v42 dst_sel:BYTE_3 dst_unused:UNUSED_PAD src0_sel:DWORD
	v_rndne_f32_e32 v46, v46
	v_med3_f32 v47, v47, s34, v20
	v_mul_f32_e32 v49, v32, v49
	v_cvt_i32_f32_sdwa v58, v58 dst_sel:BYTE_3 dst_unused:UNUSED_PAD src0_sel:DWORD
	v_rndne_f32_e32 v62, v62
	v_med3_f32 v63, v63, s34, v20
	v_mul_f32_e32 v65, v32, v65
	v_cvt_i32_f32_e32 v64, v64
	v_cvt_i32_f32_sdwa v70, v70 dst_sel:WORD_1 dst_unused:UNUSED_PAD src0_sel:DWORD
	v_rndne_f32_e32 v67, v67
	v_rndne_f32_e32 v75, v75
	v_med3_f32 v68, v68, s34, v20
	v_med3_f32 v76, v76, s34, v20
	v_mul_f32_e32 v69, v32, v69
	v_mul_f32_e32 v77, v32, v77
	v_cvt_i32_f32_e32 v80, v80
	v_cvt_i32_f32_sdwa v86, v86 dst_sel:WORD_1 dst_unused:UNUSED_PAD src0_sel:DWORD
	v_rndne_f32_e32 v83, v83
	v_rndne_f32_e32 v90, v90
	v_med3_f32 v84, v84, s34, v20
	v_med3_f32 v91, v91, s34, v20
	v_mul_f32_e32 v85, v32, v85
	v_mul_f32_e32 v92, v32, v93
	v_cvt_i32_f32_e32 v35, v35
	v_rndne_f32_e32 v36, v36
	v_rndne_f32_e32 v44, v44
	v_med3_f32 v37, v37, s34, v20
	v_med3_f32 v45, v45, s34, v20
	v_cvt_i32_f32_e32 v51, v51
	v_cvt_i32_f32_sdwa v59, v59 dst_sel:WORD_1 dst_unused:UNUSED_PAD src0_sel:DWORD
	v_rndne_f32_e32 v52, v52
	v_rndne_f32_e32 v60, v60
	v_med3_f32 v53, v53, s34, v20
	v_med3_f32 v61, v61, s34, v20
	v_cvt_i32_f32_e32 v71, v71
	v_rndne_f32_e32 v72, v72
	v_med3_f32 v73, v73, s34, v20
	v_cvt_i32_f32_e32 v87, v87
	v_rndne_f32_e32 v88, v88
	v_med3_f32 v89, v89, s34, v20
	v_cvt_i32_f32_e32 v40, v40
	v_rndne_f32_e32 v41, v41
	v_cvt_i32_f32_e32 v56, v56
	v_rndne_f32_e32 v57, v57
	v_cvt_i32_f32_sdwa v74, v74 dst_sel:BYTE_3 dst_unused:UNUSED_PAD src0_sel:DWORD
	v_rndne_f32_e32 v78, v78
	v_med3_f32 v79, v79, s34, v20
	v_mul_f32_e32 v81, v32, v81
	v_cvt_i32_f32_sdwa v29, v29 dst_sel:BYTE_3 dst_unused:UNUSED_PAD src0_sel:DWORD
	v_rndne_f32_e32 v30, v30
	v_med3_f32 v31, v31, s34, v20
	v_mul_f32_e32 v32, v32, v97
	v_cvt_i32_f32_sdwa v46, v46 dst_sel:BYTE_3 dst_unused:UNUSED_PAD src0_sel:DWORD
	v_rndne_f32_e32 v47, v47
	v_med3_f32 v49, v49, s34, v20
	v_cvt_i32_f32_sdwa v62, v62 dst_sel:BYTE_3 dst_unused:UNUSED_PAD src0_sel:DWORD
	v_rndne_f32_e32 v63, v63
	v_med3_f32 v65, v65, s34, v20
	v_cvt_i32_f32_e32 v67, v67
	v_cvt_i32_f32_sdwa v75, v75 dst_sel:WORD_1 dst_unused:UNUSED_PAD src0_sel:DWORD
	v_rndne_f32_e32 v68, v68
	v_rndne_f32_e32 v76, v76
	v_med3_f32 v69, v69, s34, v20
	v_med3_f32 v77, v77, s34, v20
	v_cvt_i32_f32_e32 v83, v83
	v_cvt_i32_f32_sdwa v90, v90 dst_sel:WORD_1 dst_unused:UNUSED_PAD src0_sel:DWORD
	v_rndne_f32_e32 v84, v84
	v_rndne_f32_e32 v91, v91
	v_med3_f32 v85, v85, s34, v20
	v_med3_f32 v92, v92, s34, v20
	v_cvt_i32_f32_e32 v36, v36
	v_cvt_i32_f32_sdwa v44, v44 dst_sel:WORD_1 dst_unused:UNUSED_PAD src0_sel:DWORD
	v_rndne_f32_e32 v37, v37
	v_rndne_f32_e32 v45, v45
	v_cvt_i32_f32_e32 v52, v52
	v_cvt_i32_f32_sdwa v60, v60 dst_sel:WORD_1 dst_unused:UNUSED_PAD src0_sel:DWORD
	v_rndne_f32_e32 v53, v53
	v_rndne_f32_e32 v61, v61
	v_cvt_i32_f32_e32 v72, v72
	v_rndne_f32_e32 v73, v73
	v_cvt_i32_f32_e32 v88, v88
	v_rndne_f32_e32 v89, v89
	v_cvt_i32_f32_e32 v41, v41
	v_cvt_i32_f32_e32 v57, v57
	v_cvt_i32_f32_sdwa v78, v78 dst_sel:BYTE_3 dst_unused:UNUSED_PAD src0_sel:DWORD
	v_rndne_f32_e32 v79, v79
	v_med3_f32 v81, v81, s34, v20
	v_cvt_i32_f32_sdwa v30, v30 dst_sel:BYTE_3 dst_unused:UNUSED_PAD src0_sel:DWORD
	v_rndne_f32_e32 v31, v31
	v_med3_f32 v32, v32, s34, v20
	v_cvt_i32_f32_sdwa v47, v47 dst_sel:BYTE_3 dst_unused:UNUSED_PAD src0_sel:DWORD
	v_rndne_f32_e32 v49, v49
	v_cvt_i32_f32_sdwa v63, v63 dst_sel:BYTE_3 dst_unused:UNUSED_PAD src0_sel:DWORD
	v_rndne_f32_e32 v65, v65
	v_cvt_i32_f32_e32 v68, v68
	v_cvt_i32_f32_sdwa v76, v76 dst_sel:WORD_1 dst_unused:UNUSED_PAD src0_sel:DWORD
	v_rndne_f32_e32 v69, v69
	v_rndne_f32_e32 v77, v77
	v_cvt_i32_f32_e32 v84, v84
	v_cvt_i32_f32_sdwa v91, v91 dst_sel:WORD_1 dst_unused:UNUSED_PAD src0_sel:DWORD
	v_rndne_f32_e32 v85, v85
	v_rndne_f32_e32 v92, v92
	v_cvt_i32_f32_e32 v37, v37
	v_cvt_i32_f32_sdwa v45, v45 dst_sel:WORD_1 dst_unused:UNUSED_PAD src0_sel:DWORD
	v_cvt_i32_f32_e32 v53, v53
	v_cvt_i32_f32_sdwa v61, v61 dst_sel:WORD_1 dst_unused:UNUSED_PAD src0_sel:DWORD
	v_cvt_i32_f32_e32 v73, v73
	v_cvt_i32_f32_e32 v89, v89
	v_lshlrev_b32_e32 v34, 8, v34
	v_lshlrev_b32_e32 v50, 8, v50
	v_cvt_i32_f32_sdwa v79, v79 dst_sel:BYTE_3 dst_unused:UNUSED_PAD src0_sel:DWORD
	v_rndne_f32_e32 v81, v81
	v_cvt_i32_f32_sdwa v31, v31 dst_sel:BYTE_3 dst_unused:UNUSED_PAD src0_sel:DWORD
	v_rndne_f32_e32 v32, v32
	v_cvt_i32_f32_sdwa v49, v49 dst_sel:BYTE_3 dst_unused:UNUSED_PAD src0_sel:DWORD
	v_cvt_i32_f32_sdwa v65, v65 dst_sel:BYTE_3 dst_unused:UNUSED_PAD src0_sel:DWORD
; __device__ __forceinline__ void cvt_item_i8(const float* src, int ld, int k0, int c0, unsigned char* dst, int Kd, int drow0, const float* cmx  , unsigned char* scr, int lane) {
;     ...
; #pragma unroll
;     for (int g = 0; g < 4; ++g)
; #pragma unroll
;         for (int i = 0; i < 4; ++i) *(unsigned*)(scr + (4 * c + i) * 132 + 32 * g + 4 * q) = pack_i8x4(v[g][0][i] * inv[i], v[g][1][i] * inv[i], v[g][2][i] * inv[i], v[g][3][i] * inv[i]);
;     asm volatile("s_waitcnt lgkmcnt(0)" ::: "memory");
; #pragma unroll
;     for (int r = 0; r < 4; ++r) { const int n = 8 * r + (lane >> 3), ch = lane & 7; const unsigned char* p = scr + n * 132 + ch * 16;
;         u32x4 o; o.x = *(const unsigned*)(p); o.y = *(const unsigned*)(p + 4); o.z = *(const unsigned*)(p + 8); o.w = *(const unsigned*)(p + 12);
;         *(u32x4*)(dst + (size_t)(drow0 + n) * Kd + k0 + 16 * ch) = o; }
;     asm volatile("s_waitcnt lgkmcnt(0)" ::: "memory");
;     ...
;     for (int it = first + F.gw; it < N; it += F.NGW) conv_item<GRP>(F, it);
	v_cvt_i32_f32_e32 v69, v69
	v_cvt_i32_f32_sdwa v77, v77 dst_sel:WORD_1 dst_unused:UNUSED_PAD src0_sel:DWORD
	v_cvt_i32_f32_e32 v85, v85
	v_cvt_i32_f32_sdwa v92, v92 dst_sel:WORD_1 dst_unused:UNUSED_PAD src0_sel:DWORD
	v_and_b32_e32 v38, 0xff0000, v38
	v_and_b32_e32 v54, 0xff0000, v54
	v_lshlrev_b32_e32 v66, 8, v66
	v_lshlrev_b32_e32 v82, 8, v82
	v_perm_b32 v33, v34, v33, s35
	v_lshlrev_b32_e32 v34, 8, v39
	v_and_b32_e32 v39, 0xff0000, v43
	v_perm_b32 v43, v50, v48, s35
	v_lshlrev_b32_e32 v48, 8, v55
	v_cvt_i32_f32_sdwa v81, v81 dst_sel:BYTE_3 dst_unused:UNUSED_PAD src0_sel:DWORD
	v_cvt_i32_f32_sdwa v32, v32 dst_sel:BYTE_3 dst_unused:UNUSED_PAD src0_sel:DWORD
	v_and_b32_e32 v70, 0xff0000, v70
	v_and_b32_e32 v86, 0xff0000, v86
	v_and_b32_e32 v50, 0xff0000, v59
	v_perm_b32 v55, v66, v64, s35
	v_lshlrev_b32_e32 v59, 8, v71
	v_perm_b32 v66, v82, v80, s35
	v_lshlrev_b32_e32 v71, 8, v87
	v_or3_b32 v33, v33, v38, v42
	v_perm_b32 v34, v34, v35, s35
	v_lshlrev_b32_e32 v35, 8, v40
	v_or3_b32 v40, v43, v54, v58
	v_perm_b32 v42, v48, v51, s35
	v_lshlrev_b32_e32 v43, 8, v56
	v_and_b32_e32 v64, 0xff0000, v75
	v_and_b32_e32 v75, 0xff0000, v90
	v_and_b32_e32 v38, 0xff0000, v44
	v_and_b32_e32 v44, 0xff0000, v60
	v_or3_b32 v48, v55, v70, v74
	v_perm_b32 v51, v59, v67, s35
	v_lshlrev_b32_e32 v54, 8, v72
	v_or3_b32 v29, v66, v86, v29
	v_perm_b32 v56, v71, v83, s35
	v_lshlrev_b32_e32 v58, 8, v88
	v_or3_b32 v34, v34, v39, v46
	v_perm_b32 v35, v35, v36, s35
	v_lshlrev_b32_e32 v36, 8, v41
	ds_write2_b32 v21, v33, v40 offset1:8
	v_or3_b32 v33, v42, v50, v62
	v_perm_b32 v40, v43, v52, s35
	v_lshlrev_b32_e32 v41, 8, v57
	v_and_b32_e32 v55, 0xff0000, v76
	v_and_b32_e32 v59, 0xff0000, v91
	v_and_b32_e32 v39, 0xff0000, v45
	v_and_b32_e32 v42, 0xff0000, v61
	v_or3_b32 v43, v51, v64, v78
	v_perm_b32 v45, v54, v68, s35
	v_lshlrev_b32_e32 v46, 8, v73
	ds_write2_b32 v21, v48, v29 offset0:16 offset1:24
	v_or3_b32 v29, v56, v75, v30
	v_perm_b32 v30, v58, v84, s35
	v_lshlrev_b32_e32 v48, 8, v89
	v_or3_b32 v35, v35, v38, v47
	v_perm_b32 v36, v36, v37, s35
	ds_write2_b32 v21, v34, v33 offset0:33 offset1:41
	v_or3_b32 v33, v40, v44, v63
	v_perm_b32 v34, v41, v53, s35
	v_and_b32_e32 v50, 0xff0000, v77
	v_and_b32_e32 v51, 0xff0000, v92
	v_or3_b32 v37, v45, v55, v79
	v_perm_b32 v38, v46, v69, s35
	ds_write2_b32 v21, v43, v29 offset0:49 offset1:57
	v_or3_b32 v29, v30, v59, v31
	v_perm_b32 v30, v48, v85, s35
	v_or3_b32 v31, v36, v39, v49
	ds_write2_b32 v21, v35, v33 offset0:66 offset1:74
	v_or3_b32 v33, v34, v42, v65
	v_or3_b32 v34, v38, v50, v81
	ds_write2_b32 v21, v37, v29 offset0:82 offset1:90
	v_or3_b32 v29, v30, v51, v32
	ds_write2_b32 v21, v31, v33 offset0:99 offset1:107
	ds_write2_b32 v21, v34, v29 offset0:115 offset1:123
	s_waitcnt lgkmcnt(0)
	ds_read2_b32 v[30:31], v22 offset1:1
	ds_read2_b32 v[32:33], v22 offset0:2 offset1:3
	ds_read2_b32 v[34:35], v23 offset1:1
	ds_read2_b32 v[36:37], v24 offset1:1
	ds_read2_b32 v[38:39], v25 offset1:1
	ds_read2_b32 v[40:41], v26 offset1:1
	ds_read2_b32 v[42:43], v27 offset1:1
	ds_read2_b32 v[44:45], v28 offset1:1
	s_waitcnt lgkmcnt(6)
	global_store_dwordx4 v[10:11], v[30:33], off
	s_waitcnt lgkmcnt(4)
	global_store_dwordx4 v[12:13], v[34:37], off
	s_waitcnt lgkmcnt(2)
	global_store_dwordx4 v[14:15], v[38:41], off
	s_waitcnt lgkmcnt(0)
	global_store_dwordx4 v[6:7], v[42:45], off
	s_waitcnt lgkmcnt(0)
	s_bitcmp0_b32 s100, 0
	s_cbranch_scc1 .Lcv1_exit
	s_waitcnt vmcnt(4)
	v_mov_b64_e32 v[6:7], v[128:129]
	v_mov_b64_e32 v[10:11], v[132:133]
	v_mov_b64_e32 v[12:13], v[134:135]
	v_mov_b64_e32 v[14:15], v[136:137]
	v_mov_b64_e32 v[30:31], v[120:121]
	v_mov_b64_e32 v[32:33], v[122:123]
	v_mov_b64_e32 v[34:35], v[144:145]
	v_mov_b64_e32 v[36:37], v[146:147]
	v_mov_b64_e32 v[38:39], v[148:149]
	v_mov_b64_e32 v[40:41], v[150:151]
	v_mov_b64_e32 v[42:43], v[152:153]
	v_mov_b64_e32 v[44:45], v[154:155]
	v_mov_b64_e32 v[46:47], v[156:157]
	v_mov_b64_e32 v[48:49], v[158:159]
	v_mov_b64_e32 v[50:51], v[160:161]
	v_mov_b64_e32 v[52:53], v[162:163]
	v_mov_b64_e32 v[54:55], v[164:165]
	v_mov_b64_e32 v[56:57], v[166:167]
	v_mov_b64_e32 v[58:59], v[168:169]
	v_mov_b64_e32 v[60:61], v[170:171]
	v_mov_b64_e32 v[62:63], v[172:173]
	v_mov_b64_e32 v[64:65], v[174:175]
	v_mov_b64_e32 v[66:67], v[176:177]
	v_mov_b64_e32 v[68:69], v[178:179]
	v_mov_b64_e32 v[70:71], v[180:181]
	v_mov_b64_e32 v[72:73], v[182:183]
	v_mov_b64_e32 v[74:75], v[184:185]
	v_mov_b64_e32 v[76:77], v[186:187]
	v_mov_b64_e32 v[78:79], v[188:189]
	v_mov_b64_e32 v[80:81], v[190:191]
	v_mov_b64_e32 v[82:83], v[210:211]
	v_mov_b64_e32 v[84:85], v[212:213]
	v_mov_b64_e32 v[86:87], v[214:215]
	v_mov_b64_e32 v[88:89], v[216:217]
	v_mov_b64_e32 v[90:91], v[218:219]
	v_mov_b64_e32 v[92:93], v[220:221]
	v_mov_b64_e32 v[94:95], v[222:223]
	v_mov_b64_e32 v[96:97], v[224:225]
	s_lshr_b32 s100, s100, 1
	s_branch .Lcv1_R
.Lcv1_exit:
.LBB0_1673:
	s_barrier

; __device__ __forceinline__ void cvt_item_i8(const float* src, int ld, int k0, int c0, unsigned char* dst, int Kd, int drow0, const float* cmx  , unsigned char* scr, int lane) {
;     const int c = lane & 7, q = lane >> 3;
;     const f32x4 cm = *(const f32x4*)(cmx + 4 * c);
;     f32x4 inv; inv[0] = cm[0] > 0.f ? 127.f / cm[0] : 0.f; inv[1] = cm[1] > 0.f ? 127.f / cm[1] : 0.f; inv[2] = cm[2] > 0.f ? 127.f / cm[2] : 0.f; inv[3] = cm[3] > 0.f ? 127.f / cm[3] : 0.f;
;     f32x4 v[4][4];
; #pragma unroll
;     for (int g = 0; g < 4; ++g)
; #pragma unroll
;         for (int j = 0; j < 4; ++j) v[g][j] = __builtin_nontemporal_load((const f32x4*)(src + (size_t)(k0 + 32 * g + 4 * q + j) * ld + c0 + 4 * c));
; template <int GRP>
; __device__ __forceinline__ void conv_item(Frame& F, int r) {
;     ...
;     else { constexpr int KBN = (GRP == 3) ? 16 : CMS_KB, I_E = KBN * 88; const int up = r / (8 * I_E); r %= (8 * I_E); const int e = r / I_E; r %= I_E; const int kb = r / 88, nb = r % 88, n0 = nb * 32, drow = (n0 >> 7) * 256 + up * 128 + (n0 & 127);
;         if (GRP == 3) cvt_item_i8(inptr(F, up ? IN_MU : IN_MG) + (size_t)e * D * DFE, DFE, kb * 128, n0, ws + WS_MGU + (size_t)e * 2 * DFE * D, D, drow, cmx + 2 * DFF + e * 2 * DFE + drow, scr, F.lane);
;     ...
;     for (int it = first + F.gw; it < N; it += F.NGW) conv_item<GRP>(F, it);
.LBB0_1909:
	s_mul_hi_i32 s0, s3, 0x2e8ba2e9
	s_lshr_b32 s1, s0, 31
	s_ashr_i32 s0, s0, 11
	s_add_i32 s0, s0, s1
	s_mul_i32 s1, s0, 0xffffd400
	s_lshl_b32 s6, s0, 7
	s_add_i32 s0, s3, s1
	s_mul_i32 s1, s0, 0xba3
	s_lshr_b32 s7, s1, 31
	s_ashr_i32 s1, s1, 22
	s_add_i32 s1, s1, s7
	s_mul_i32 s7, s1, 0x580
	s_sub_i32 s0, s0, s7
	s_sext_i32_i16 s38, s0
	s_mulk_i32 s38, 0xba3
	s_lshr_b32 s40, s38, 31
	s_ashr_i32 s38, s38, 18
	s_add_i32 s40, s38, s40
	s_sext_i32_i16 s38, s40
	s_mulk_i32 s40, 0x58
	s_sub_i32 s0, s0, s40
	s_sext_i32_i16 s40, s0
	s_lshl_b32 s0, s40, 5
	s_lshl_b32 s40, s40, 6
	s_and_b32 s40, s40, 0xffffff00
	s_and_b32 s41, s0, 0x60
	s_add_i32 s40, s40, s6
	s_add_i32 s39, s3, 0x2bff
	s_or_b32 s6, s40, s41
	s_cmpk_lt_u32 s39, 0x57ff
	s_cselect_b32 s39, s15, 0xa8
	v_or_b32_e32 v8, s6, v17
	s_add_i32 s39, s39, 0
	v_ashrrev_i32_e32 v9, 31, v8
	s_add_i32 s39, s39, 0x20200
	v_lshlrev_b64 v[98:99], 11, v[8:9]
	v_mov_b32_e32 v8, s39
	ds_read_b64 v[8:9], v8
	s_sext_i32_i16 s11, s1
	s_mul_i32 s9, s11, 0x1600000
	s_mul_hi_i32 s1, s11, 0x1600000
	s_mul_i32 s10, s11, 0xb00000
	s_waitcnt lgkmcnt(0)
	v_readfirstlane_b32 s39, v8
	v_readfirstlane_b32 s40, v9
	s_add_u32 s9, s39, s9
	s_addc_u32 s39, s40, s1
	s_lshl_b32 s38, s38, 7
	s_mul_hi_i32 s7, s11, 0xb00000
	s_add_u32 s10, s4, s10
	s_mul_hi_i32 s8, s11, 0x5800
	s_mulk_i32 s11, 0x5800
	s_addc_u32 s40, s12, s7
	s_add_u32 s1, s13, s11
	s_addc_u32 s8, s14, s8
	s_ashr_i32 s7, s6, 31
	v_or_b32_e32 v6, s6, v1
	v_or_b32_e32 v10, s6, v18
	v_or_b32_e32 v12, s6, v19
	s_lshl_b64 s[6:7], s[6:7], 2
	s_add_u32 s6, s1, s6
	s_addc_u32 s7, s8, s7
	s_ashr_i32 s1, s0, 31
	s_lshl_b64 s[0:1], s[0:1], 2
	v_or_b32_e32 v8, s38, v16
	s_add_u32 s0, s9, s0
	v_ashrrev_i32_e32 v11, 31, v10
	v_mul_i32_i24_e32 v8, 0x2c00, v8
	s_addc_u32 s1, s39, s1
	v_lshlrev_b64 v[100:101], 11, v[10:11]
	v_ashrrev_i32_e32 v9, 31, v8
	v_lshl_add_u64 v[10:11], s[0:1], 0, v[4:5]
	v_ashrrev_i32_e32 v7, 31, v6
	v_ashrrev_i32_e32 v13, 31, v12
	v_lshl_add_u64 v[10:11], v[10:11], 0, v[8:9]
	v_lshlrev_b64 v[14:15], 11, v[6:7]
	v_lshlrev_b64 v[6:7], 11, v[12:13]
	v_add_co_u32_e32 v12, vcc, s17, v10
	global_load_dwordx4 v[30:33], v4, s[6:7]
	s_nop 0
	v_addc_co_u32_e32 v13, vcc, 0, v11, vcc
	v_add_co_u32_e32 v42, vcc, s20, v10
	s_ashr_i32 s6, s38, 31
	s_nop 0
	v_addc_co_u32_e32 v43, vcc, 0, v11, vcc
	v_add_co_u32_e32 v46, vcc, s21, v10
	s_add_u32 s0, s10, s38
	s_nop 0
	v_addc_co_u32_e32 v47, vcc, 0, v11, vcc
	v_add_co_u32_e32 v50, vcc, s22, v10
	s_addc_u32 s1, s40, s6
	s_nop 0
	v_addc_co_u32_e32 v51, vcc, 0, v11, vcc
	v_add_co_u32_e32 v54, vcc, s23, v10
	v_lshl_add_u64 v[8:9], s[0:1], 0, v[2:3]
	s_nop 0
	v_addc_co_u32_e32 v55, vcc, 0, v11, vcc
	v_add_co_u32_e32 v58, vcc, s24, v10
	v_lshl_add_u64 v[6:7], v[8:9], 0, v[6:7]
	s_nop 0
	v_addc_co_u32_e32 v59, vcc, 0, v11, vcc
	v_add_co_u32_e32 v62, vcc, s25, v10
	s_add_i32 s3, s3, s42
	s_nop 0
	v_addc_co_u32_e32 v63, vcc, 0, v11, vcc
	v_add_co_u32_e32 v66, vcc, s26, v10
	s_cmpk_lt_i32 s3, 0x5800
	s_nop 0
	v_addc_co_u32_e32 v67, vcc, 0, v11, vcc
	v_add_co_u32_e32 v70, vcc, s27, v10
	s_nop 0
	s_nop 0
	v_addc_co_u32_e32 v71, vcc, 0, v11, vcc
	v_add_co_u32_e32 v74, vcc, s28, v10
	s_nop 0
	s_nop 0
	v_addc_co_u32_e32 v75, vcc, 0, v11, vcc
	v_add_co_u32_e32 v78, vcc, s29, v10
	s_nop 0
	s_nop 0
	v_addc_co_u32_e32 v79, vcc, 0, v11, vcc
	v_add_co_u32_e32 v82, vcc, s30, v10
	s_nop 0
	s_nop 0
	v_addc_co_u32_e32 v83, vcc, 0, v11, vcc
	v_add_co_u32_e32 v86, vcc, s31, v10
	s_nop 0
	s_nop 0
	v_addc_co_u32_e32 v87, vcc, 0, v11, vcc
	v_add_co_u32_e32 v90, vcc, s34, v10
	s_nop 0
	s_nop 0
	v_addc_co_u32_e32 v91, vcc, 0, v11, vcc
	v_add_co_u32_e32 v94, vcc, s35, v10
	s_nop 0
	s_nop 0
	v_addc_co_u32_e32 v95, vcc, 0, v11, vcc
	global_load_dwordx4 v[34:37], v[10:11], off nt
	global_load_dwordx4 v[38:41], v[12:13], off offset:3072 nt
	s_nop 0
	global_load_dwordx4 v[42:45], v[42:43], off offset:2048 nt
	s_nop 0
	global_load_dwordx4 v[46:49], v[46:47], off offset:1024 nt
	s_nop 0
	global_load_dwordx4 v[50:53], v[50:51], off nt
	s_nop 0
	global_load_dwordx4 v[54:57], v[54:55], off offset:3072 nt
	s_nop 0
	global_load_dwordx4 v[58:61], v[58:59], off offset:2048 nt
	s_nop 0
	global_load_dwordx4 v[62:65], v[62:63], off offset:1024 nt
	s_nop 0
	global_load_dwordx4 v[66:69], v[66:67], off nt
	s_nop 0
	global_load_dwordx4 v[70:73], v[70:71], off offset:3072 nt
	s_nop 0
	global_load_dwordx4 v[74:77], v[74:75], off offset:2048 nt
	s_nop 0
	global_load_dwordx4 v[78:81], v[78:79], off offset:1024 nt
	s_nop 0
	global_load_dwordx4 v[82:85], v[82:83], off nt
	s_nop 0
	global_load_dwordx4 v[86:89], v[86:87], off offset:3072 nt
	s_nop 0
	global_load_dwordx4 v[90:93], v[90:91], off offset:2048 nt
	s_nop 0
	global_load_dwordx4 v[94:97], v[94:95], off offset:1024 nt
	s_cselect_b32 s100, 1, 0
	v_lshl_add_u64 v[12:13], v[8:9], 0, v[98:99]
	v_lshl_add_u64 v[10:11], v[8:9], 0, v[14:15]
	v_lshl_add_u64 v[14:15], v[8:9], 0, v[100:101]
	s_waitcnt vmcnt(0)
; __device__ __forceinline__ void cvt_item_i8(const float* src, int ld, int k0, int c0, unsigned char* dst, int Kd, int drow0, const float* cmx  , unsigned char* scr, int lane) {
;     const int c = lane & 7, q = lane >> 3;
;     const f32x4 cm = *(const f32x4*)(cmx + 4 * c);
;     f32x4 inv; inv[0] = cm[0] > 0.f ? 127.f / cm[0] : 0.f; inv[1] = cm[1] > 0.f ? 127.f / cm[1] : 0.f; inv[2] = cm[2] > 0.f ? 127.f / cm[2] : 0.f; inv[3] = cm[3] > 0.f ? 127.f / cm[3] : 0.f;
;     f32x4 v[4][4];
; #pragma unroll
;     for (int g = 0; g < 4; ++g)
; #pragma unroll
;         for (int j = 0; j < 4; ++j) v[g][j] = __builtin_nontemporal_load((const f32x4*)(src + (size_t)(k0 + 32 * g + 4 * q + j) * ld + c0 + 4 * c));
; template <int GRP>
; __device__ __forceinline__ void conv_item(Frame& F, int r) {
;     ...
;     else { constexpr int KBN = (GRP == 3) ? 16 : CMS_KB, I_E = KBN * 88; const int up = r / (8 * I_E); r %= (8 * I_E); const int e = r / I_E; r %= I_E; const int kb = r / 88, nb = r % 88, n0 = nb * 32, drow = (n0 >> 7) * 256 + up * 128 + (n0 & 127);
;         if (GRP == 3) cvt_item_i8(inptr(F, up ? IN_MU : IN_MG) + (size_t)e * D * DFE, DFE, kb * 128, n0, ws + WS_MGU + (size_t)e * 2 * DFE * D, D, drow, cmx + 2 * DFF + e * 2 * DFE + drow, scr, F.lane);
;     ...
;     for (int it = first + F.gw; it < N; it += F.NGW) conv_item<GRP>(F, it);
.Lcv3_R:
	s_bitcmp0_b32 s100, 0
	s_cbranch_scc1 .Lcv3_noP
	s_mul_hi_i32 s0, s3, 0x2e8ba2e9
	s_lshr_b32 s1, s0, 31
	s_ashr_i32 s0, s0, 11
	s_add_i32 s0, s0, s1
	s_mul_i32 s1, s0, 0xffffd400
	s_lshl_b32 s6, s0, 7
	s_add_i32 s0, s3, s1
	s_mul_i32 s1, s0, 0xba3
	s_lshr_b32 s7, s1, 31
	s_ashr_i32 s1, s1, 22
	s_add_i32 s1, s1, s7
	s_mul_i32 s7, s1, 0x580
	s_sub_i32 s0, s0, s7
	s_sext_i32_i16 s38, s0
	s_mulk_i32 s38, 0xba3
	s_lshr_b32 s40, s38, 31
	s_ashr_i32 s38, s38, 18
	s_add_i32 s40, s38, s40
	s_sext_i32_i16 s38, s40
	s_mulk_i32 s40, 0x58
	s_sub_i32 s0, s0, s40
	s_sext_i32_i16 s40, s0
	s_lshl_b32 s0, s40, 5
	s_lshl_b32 s40, s40, 6
	s_and_b32 s40, s40, 0xffffff00
	s_and_b32 s41, s0, 0x60
	s_add_i32 s40, s40, s6
	s_add_i32 s39, s3, 0x2bff
	s_or_b32 s6, s40, s41
	s_cmpk_lt_u32 s39, 0x57ff
	s_cselect_b32 s39, s15, 0xa8
	v_or_b32_e32 v130, s6, v17
	s_add_i32 s39, s39, 0
	v_ashrrev_i32_e32 v131, 31, v130
	s_add_i32 s39, s39, 0x20200
	v_lshlrev_b64 v[124:125], 11, v[130:131]
	v_mov_b32_e32 v130, s39
	ds_read_b64 v[130:131], v130
	s_sext_i32_i16 s11, s1
	s_mul_i32 s9, s11, 0x1600000
	s_mul_hi_i32 s1, s11, 0x1600000
	s_mul_i32 s10, s11, 0xb00000
	s_waitcnt lgkmcnt(0)
	v_readfirstlane_b32 s39, v130
	v_readfirstlane_b32 s40, v131
	s_add_u32 s9, s39, s9
	s_addc_u32 s39, s40, s1
	s_lshl_b32 s38, s38, 7
	s_mul_hi_i32 s7, s11, 0xb00000
	s_add_u32 s10, s4, s10
	s_mul_hi_i32 s8, s11, 0x5800
	s_mulk_i32 s11, 0x5800
	s_addc_u32 s40, s12, s7
	s_add_u32 s1, s13, s11
	s_addc_u32 s8, s14, s8
	s_ashr_i32 s7, s6, 31
	v_or_b32_e32 v128, s6, v1
	v_or_b32_e32 v132, s6, v18
	v_or_b32_e32 v134, s6, v19
	s_lshl_b64 s[6:7], s[6:7], 2
	s_add_u32 s6, s1, s6
	s_addc_u32 s7, s8, s7
	s_ashr_i32 s1, s0, 31
	s_lshl_b64 s[0:1], s[0:1], 2
	v_or_b32_e32 v130, s38, v16
	s_add_u32 s0, s9, s0
	v_ashrrev_i32_e32 v133, 31, v132
	v_mul_i32_i24_e32 v130, 0x2c00, v130
	s_addc_u32 s1, s39, s1
	v_lshlrev_b64 v[126:127], 11, v[132:133]
	v_ashrrev_i32_e32 v131, 31, v130
	v_lshl_add_u64 v[132:133], s[0:1], 0, v[4:5]
	v_ashrrev_i32_e32 v129, 31, v128
	v_ashrrev_i32_e32 v135, 31, v134
	v_lshl_add_u64 v[132:133], v[132:133], 0, v[130:131]
	v_lshlrev_b64 v[136:137], 11, v[128:129]
	v_lshlrev_b64 v[128:129], 11, v[134:135]
	v_add_co_u32_e32 v134, vcc, s17, v132
	global_load_dwordx4 v[120:123], v4, s[6:7]
	s_nop 0
	v_addc_co_u32_e32 v135, vcc, 0, v133, vcc
	v_add_co_u32_e32 v152, vcc, s20, v132
	s_ashr_i32 s6, s38, 31
	s_nop 0
	v_addc_co_u32_e32 v153, vcc, 0, v133, vcc
	v_add_co_u32_e32 v156, vcc, s21, v132
	s_add_u32 s0, s10, s38
	s_nop 0
	v_addc_co_u32_e32 v157, vcc, 0, v133, vcc
	v_add_co_u32_e32 v160, vcc, s22, v132
	s_addc_u32 s1, s40, s6
	s_nop 0
	v_addc_co_u32_e32 v161, vcc, 0, v133, vcc
	v_add_co_u32_e32 v164, vcc, s23, v132
	v_lshl_add_u64 v[130:131], s[0:1], 0, v[2:3]
	s_nop 0
	v_addc_co_u32_e32 v165, vcc, 0, v133, vcc
	v_add_co_u32_e32 v168, vcc, s24, v132
	v_lshl_add_u64 v[128:129], v[130:131], 0, v[128:129]
	s_nop 0
	v_addc_co_u32_e32 v169, vcc, 0, v133, vcc
	v_add_co_u32_e32 v172, vcc, s25, v132
	s_add_i32 s3, s3, s42
	s_nop 0
	v_addc_co_u32_e32 v173, vcc, 0, v133, vcc
	v_add_co_u32_e32 v176, vcc, s26, v132
	s_cmpk_lt_i32 s3, 0x5800
	s_nop 0
	v_addc_co_u32_e32 v177, vcc, 0, v133, vcc
	v_add_co_u32_e32 v180, vcc, s27, v132
	s_nop 0
	s_nop 0
	v_addc_co_u32_e32 v181, vcc, 0, v133, vcc
	v_add_co_u32_e32 v184, vcc, s28, v132
	s_nop 0
	s_nop 0
	v_addc_co_u32_e32 v185, vcc, 0, v133, vcc
	v_add_co_u32_e32 v188, vcc, s29, v132
	s_nop 0
	s_nop 0
	v_addc_co_u32_e32 v189, vcc, 0, v133, vcc
	v_add_co_u32_e32 v210, vcc, s30, v132
	s_nop 0
	s_nop 0
	v_addc_co_u32_e32 v211, vcc, 0, v133, vcc
	v_add_co_u32_e32 v214, vcc, s31, v132
	s_nop 0
	s_nop 0
	v_addc_co_u32_e32 v215, vcc, 0, v133, vcc
	v_add_co_u32_e32 v218, vcc, s34, v132
	s_nop 0
	s_nop 0
	v_addc_co_u32_e32 v219, vcc, 0, v133, vcc
	v_add_co_u32_e32 v222, vcc, s35, v132
	s_nop 0
	s_nop 0
	v_addc_co_u32_e32 v223, vcc, 0, v133, vcc
	global_load_dwordx4 v[144:147], v[132:133], off nt
	global_load_dwordx4 v[148:151], v[134:135], off offset:3072 nt
	s_nop 0
	global_load_dwordx4 v[152:155], v[152:153], off offset:2048 nt
	s_nop 0
	global_load_dwordx4 v[156:159], v[156:157], off offset:1024 nt
	s_nop 0
	global_load_dwordx4 v[160:163], v[160:161], off nt
	s_nop 0
	global_load_dwordx4 v[164:167], v[164:165], off offset:3072 nt
	s_nop 0
	global_load_dwordx4 v[168:171], v[168:169], off offset:2048 nt
	s_nop 0
	global_load_dwordx4 v[172:175], v[172:173], off offset:1024 nt
	s_nop 0
	global_load_dwordx4 v[176:179], v[176:177], off nt
	s_nop 0
	global_load_dwordx4 v[180:183], v[180:181], off offset:3072 nt
	s_nop 0
	global_load_dwordx4 v[184:187], v[184:185], off offset:2048 nt
	s_nop 0
	global_load_dwordx4 v[188:191], v[188:189], off offset:1024 nt
	s_nop 0
	global_load_dwordx4 v[210:213], v[210:211], off nt
	s_nop 0
	global_load_dwordx4 v[214:217], v[214:215], off offset:3072 nt
	s_nop 0
	global_load_dwordx4 v[218:221], v[218:219], off offset:2048 nt
	s_nop 0
	global_load_dwordx4 v[222:225], v[222:223], off offset:1024 nt
	v_lshl_add_u64 v[134:135], v[130:131], 0, v[124:125]
	v_lshl_add_u64 v[132:133], v[130:131], 0, v[136:137]
	v_lshl_add_u64 v[136:137], v[130:131], 0, v[126:127]
	s_cselect_b32 s0, 2, 0
	s_or_b32 s100, s100, s0
; __device__ __forceinline__ unsigned pack_i8x4(float a, float b, float c, float d) {
;     const int ia = (int)rintf(fminf(fmaxf(a, -127.f), 127.f)), ib = (int)rintf(fminf(fmaxf(b, -127.f), 127.f)), ic = (int)rintf(fminf(fmaxf(c, -127.f), 127.f)), id = (int)rintf(fminf(fmaxf(d, -127.f), 127.f));
;     return (unsigned)(ia & 0xff) | ((unsigned)(ib & 0xff) << 8) | ((unsigned)(ic & 0xff) << 16) | ((unsigned)(id & 0xff) << 24);
; __device__ __forceinline__ void cvt_item_i8(const float* src, int ld, int k0, int c0, unsigned char* dst, int Kd, int drow0, const float* cmx  , unsigned char* scr, int lane) {
;     ...
;     f32x4 inv; inv[0] = cm[0] > 0.f ? 127.f / cm[0] : 0.f; inv[1] = cm[1] > 0.f ? 127.f / cm[1] : 0.f; inv[2] = cm[2] > 0.f ? 127.f / cm[2] : 0.f; inv[3] = cm[3] > 0.f ? 127.f / cm[3] : 0.f;
;     f32x4 v[4][4];
; #pragma unroll
;     for (int g = 0; g < 4; ++g)
; #pragma unroll
;         for (int j = 0; j < 4; ++j) v[g][j] = __builtin_nontemporal_load((const f32x4*)(src + (size_t)(k0 + 32 * g + 4 * q + j) * ld + c0 + 4 * c));
; #pragma unroll
;     for (int g = 0; g < 4; ++g)
; #pragma unroll
;         for (int i = 0; i < 4; ++i) *(unsigned*)(scr + (4 * c + i) * 132 + 32 * g + 4 * q) = pack_i8x4(v[g][0][i] * inv[i], v[g][1][i] * inv[i], v[g][2][i] * inv[i], v[g][3][i] * inv[i]);
.Lcv3_noP:
	v_div_scale_f32 v29, s[0:1], v30, v30, s16
	v_rcp_f32_e32 v105, v29
	v_div_scale_f32 v103, s[0:1], v33, v33, s16
	v_fma_f32 v109, -v29, v105, 1.0
	v_rcp_f32_e32 v108, v103
	v_fmac_f32_e32 v105, v109, v105
	v_div_scale_f32 v102, s[8:9], s16, v32, s16
	v_div_scale_f32 v99, s[0:1], v31, v31, s16
	v_rcp_f32_e32 v106, v99
	v_div_scale_f32 v101, s[0:1], v32, v32, s16
	v_rcp_f32_e32 v107, v101
	v_div_scale_f32 v98, vcc, s16, v30, s16
	v_fma_f32 v110, -v99, v106, 1.0
	v_div_scale_f32 v100, s[6:7], s16, v31, s16
	v_fmac_f32_e32 v106, v110, v106
	v_mul_f32_e32 v109, v98, v105
	v_fma_f32 v111, -v101, v107, 1.0
	v_mul_f32_e32 v110, v100, v106
	v_fma_f32 v113, -v29, v109, v98
	v_fmac_f32_e32 v107, v111, v107
	v_fma_f32 v114, -v99, v110, v100
	v_fmac_f32_e32 v109, v113, v105
	v_fma_f32 v112, -v103, v108, 1.0
	v_mul_f32_e32 v111, v102, v107
	v_fmac_f32_e32 v110, v114, v106
	v_fma_f32 v29, -v29, v109, v98
	v_div_scale_f32 v104, s[10:11], s16, v33, s16
	v_fmac_f32_e32 v108, v112, v108
	v_fma_f32 v115, -v101, v111, v102
	v_fma_f32 v98, -v99, v110, v100
	v_div_fmas_f32 v29, v29, v105, v109
	s_mov_b64 vcc, s[6:7]
	v_mul_f32_e32 v112, v104, v108
	v_fmac_f32_e32 v111, v115, v107
	v_div_fixup_f32 v29, v29, v30, s16
	v_div_fmas_f32 v98, v98, v106, v110
	v_cmp_lt_f32_e32 vcc, 0, v30
	v_fma_f32 v116, -v103, v112, v104
	v_fma_f32 v99, -v101, v111, v102
	v_cndmask_b32_e32 v29, 0, v29, vcc
	s_mov_b64 vcc, s[8:9]
	v_fmac_f32_e32 v112, v116, v108
	v_div_fixup_f32 v30, v98, v31, s16
	v_div_fmas_f32 v98, v99, v107, v111
	v_cmp_lt_f32_e32 vcc, 0, v31
	v_fma_f32 v100, -v103, v112, v104
	v_div_fixup_f32 v31, v98, v32, s16
	v_cndmask_b32_e32 v30, 0, v30, vcc
	s_mov_b64 vcc, s[10:11]
	v_div_fmas_f32 v98, v100, v108, v112
	v_cmp_lt_f32_e32 vcc, 0, v32
	v_div_fixup_f32 v32, v98, v33, s16
	s_waitcnt lgkmcnt(0)
	v_mul_f32_e32 v34, v34, v29
	v_mul_f32_e32 v38, v29, v38
	v_mul_f32_e32 v42, v29, v42
	v_mul_f32_e32 v46, v29, v46
	v_mul_f32_e32 v50, v29, v50
	v_mul_f32_e32 v54, v29, v54
	v_mul_f32_e32 v58, v29, v58
	v_mul_f32_e32 v62, v29, v62
	v_mul_f32_e32 v66, v29, v66
	v_mul_f32_e32 v70, v29, v70
	v_mul_f32_e32 v74, v29, v74
	v_mul_f32_e32 v78, v29, v78
	v_mul_f32_e32 v82, v29, v82
	v_mul_f32_e32 v86, v29, v86
	v_cndmask_b32_e32 v31, 0, v31, vcc
	v_med3_f32 v34, v34, s36, v20
	v_med3_f32 v38, v38, s36, v20
	v_med3_f32 v42, v42, s36, v20
	v_med3_f32 v46, v46, s36, v20
	v_mul_f32_e32 v39, v30, v39
	v_mul_f32_e32 v43, v30, v43
	v_mul_f32_e32 v47, v30, v47
	v_med3_f32 v50, v50, s36, v20
	v_med3_f32 v54, v54, s36, v20
	v_mul_f32_e32 v55, v30, v55
	v_cmp_lt_f32_e32 vcc, 0, v33
	v_mul_f32_e32 v90, v29, v90
	v_mul_f32_e32 v35, v35, v30
	v_med3_f32 v58, v58, s36, v20
	v_med3_f32 v62, v62, s36, v20
	v_mul_f32_e32 v51, v30, v51
	v_mul_f32_e32 v59, v30, v59
	v_mul_f32_e32 v63, v30, v63
	v_med3_f32 v66, v66, s36, v20
	v_med3_f32 v70, v70, s36, v20
	v_med3_f32 v74, v74, s36, v20
	v_med3_f32 v78, v78, s36, v20
	v_mul_f32_e32 v71, v30, v71
	v_mul_f32_e32 v79, v30, v79
	v_med3_f32 v82, v82, s36, v20
	v_med3_f32 v86, v86, s36, v20
	v_mul_f32_e32 v87, v30, v87
	v_cndmask_b32_e32 v32, 0, v32, vcc
	v_rndne_f32_e32 v33, v34
	v_rndne_f32_e32 v34, v38
	v_rndne_f32_e32 v38, v42
	v_rndne_f32_e32 v42, v46
	v_med3_f32 v39, v39, s36, v20
	v_med3_f32 v43, v43, s36, v20
	v_med3_f32 v46, v47, s36, v20
	v_mul_f32_e32 v40, v31, v40
	v_mul_f32_e32 v47, v31, v48
	v_rndne_f32_e32 v48, v50
	v_rndne_f32_e32 v50, v54
	v_med3_f32 v55, v55, s36, v20
	v_mul_f32_e32 v56, v31, v56
	v_mul_f32_e32 v29, v29, v94
	v_mul_f32_e32 v67, v30, v67
	v_mul_f32_e32 v75, v30, v75
	v_med3_f32 v90, v90, s36, v20
	v_mul_f32_e32 v83, v30, v83
	v_mul_f32_e32 v91, v30, v91
	v_med3_f32 v35, v35, s36, v20
	v_mul_f32_e32 v36, v36, v31
	v_mul_f32_e32 v44, v31, v44
	v_rndne_f32_e32 v54, v58
	v_rndne_f32_e32 v58, v62
	v_med3_f32 v51, v51, s36, v20
	v_med3_f32 v59, v59, s36, v20
	v_med3_f32 v62, v63, s36, v20
	v_mul_f32_e32 v52, v31, v52
	v_mul_f32_e32 v60, v31, v60
	v_mul_f32_e32 v63, v31, v64
	v_rndne_f32_e32 v64, v66
	v_rndne_f32_e32 v66, v70
	v_rndne_f32_e32 v70, v74
	v_rndne_f32_e32 v74, v78
	v_med3_f32 v71, v71, s36, v20
	v_med3_f32 v78, v79, s36, v20
	v_mul_f32_e32 v72, v31, v72
	v_mul_f32_e32 v79, v31, v80
	v_rndne_f32_e32 v80, v82
	v_rndne_f32_e32 v82, v86
	v_med3_f32 v87, v87, s36, v20
	v_mul_f32_e32 v88, v31, v88
	v_cvt_i32_f32_e32 v34, v34
	v_rndne_f32_e32 v39, v39
	v_rndne_f32_e32 v43, v43
	v_med3_f32 v40, v40, s36, v20
	v_mul_f32_e32 v41, v32, v41
	v_cvt_i32_f32_e32 v50, v50
	v_rndne_f32_e32 v55, v55
	v_med3_f32 v56, v56, s36, v20
	v_mul_f32_e32 v57, v32, v57
	v_med3_f32 v29, v29, s36, v20
	v_mul_f32_e32 v30, v30, v95
	v_med3_f32 v67, v67, s36, v20
	v_med3_f32 v75, v75, s36, v20
	v_mul_f32_e32 v68, v31, v68
	v_mul_f32_e32 v76, v31, v76
	v_rndne_f32_e32 v86, v90
	v_med3_f32 v83, v83, s36, v20
	v_med3_f32 v90, v91, s36, v20
	v_mul_f32_e32 v84, v31, v84
	v_mul_f32_e32 v91, v31, v92
	v_cvt_i32_f32_e32 v33, v33
	v_cvt_i32_f32_sdwa v38, v38 dst_sel:WORD_1 dst_unused:UNUSED_PAD src0_sel:DWORD
	v_rndne_f32_e32 v35, v35
	v_med3_f32 v36, v36, s36, v20
	v_med3_f32 v44, v44, s36, v20
	v_mul_f32_e32 v37, v37, v32
	v_mul_f32_e32 v45, v32, v45
	v_cvt_i32_f32_e32 v48, v48
	v_cvt_i32_f32_sdwa v54, v54 dst_sel:WORD_1 dst_unused:UNUSED_PAD src0_sel:DWORD
	v_rndne_f32_e32 v51, v51
	v_rndne_f32_e32 v59, v59
	v_med3_f32 v52, v52, s36, v20
	v_med3_f32 v60, v60, s36, v20
	v_mul_f32_e32 v53, v32, v53
	v_mul_f32_e32 v61, v32, v61
	v_cvt_i32_f32_e32 v66, v66
	v_rndne_f32_e32 v71, v71
	v_med3_f32 v72, v72, s36, v20
	v_mul_f32_e32 v73, v32, v73
	v_cvt_i32_f32_e32 v82, v82
	v_rndne_f32_e32 v87, v87
	v_med3_f32 v88, v88, s36, v20
	v_mul_f32_e32 v89, v32, v89
; __device__ __forceinline__ unsigned pack_i8x4(float a, float b, float c, float d) {
;     const int ia = (int)rintf(fminf(fmaxf(a, -127.f), 127.f)), ib = (int)rintf(fminf(fmaxf(b, -127.f), 127.f)), ic = (int)rintf(fminf(fmaxf(c, -127.f), 127.f)), id = (int)rintf(fminf(fmaxf(d, -127.f), 127.f));
;     return (unsigned)(ia & 0xff) | ((unsigned)(ib & 0xff) << 8) | ((unsigned)(ic & 0xff) << 16) | ((unsigned)(id & 0xff) << 24);
; __device__ __forceinline__ void cvt_item_i8(const float* src, int ld, int k0, int c0, unsigned char* dst, int Kd, int drow0, const float* cmx  , unsigned char* scr, int lane) {
;     ...
; #pragma unroll
;     for (int g = 0; g < 4; ++g)
; #pragma unroll
;         for (int i = 0; i < 4; ++i) *(unsigned*)(scr + (4 * c + i) * 132 + 32 * g + 4 * q) = pack_i8x4(v[g][0][i] * inv[i], v[g][1][i] * inv[i], v[g][2][i] * inv[i], v[g][3][i] * inv[i]);
	v_cvt_i32_f32_e32 v39, v39
	v_cvt_i32_f32_sdwa v43, v43 dst_sel:WORD_1 dst_unused:UNUSED_PAD src0_sel:DWORD
	v_rndne_f32_e32 v40, v40
	v_med3_f32 v41, v41, s36, v20
	v_cvt_i32_f32_e32 v55, v55
	v_rndne_f32_e32 v56, v56
	v_med3_f32 v57, v57, s36, v20
	v_rndne_f32_e32 v29, v29
	v_med3_f32 v30, v30, s36, v20
	v_mul_f32_e32 v31, v31, v96
	v_cvt_i32_f32_sdwa v42, v42 dst_sel:BYTE_3 dst_unused:UNUSED_PAD src0_sel:DWORD
	v_rndne_f32_e32 v46, v46
	v_med3_f32 v47, v47, s36, v20
	v_mul_f32_e32 v49, v32, v49
	v_cvt_i32_f32_sdwa v58, v58 dst_sel:BYTE_3 dst_unused:UNUSED_PAD src0_sel:DWORD
	v_rndne_f32_e32 v62, v62
	v_med3_f32 v63, v63, s36, v20
	v_mul_f32_e32 v65, v32, v65
	v_cvt_i32_f32_e32 v64, v64
	v_cvt_i32_f32_sdwa v70, v70 dst_sel:WORD_1 dst_unused:UNUSED_PAD src0_sel:DWORD
	v_rndne_f32_e32 v67, v67
	v_rndne_f32_e32 v75, v75
	v_med3_f32 v68, v68, s36, v20
	v_med3_f32 v76, v76, s36, v20
	v_mul_f32_e32 v69, v32, v69
	v_mul_f32_e32 v77, v32, v77
	v_cvt_i32_f32_e32 v80, v80
	v_cvt_i32_f32_sdwa v86, v86 dst_sel:WORD_1 dst_unused:UNUSED_PAD src0_sel:DWORD
	v_rndne_f32_e32 v83, v83
	v_rndne_f32_e32 v90, v90
	v_med3_f32 v84, v84, s36, v20
	v_med3_f32 v91, v91, s36, v20
	v_mul_f32_e32 v85, v32, v85
	v_mul_f32_e32 v92, v32, v93
	v_cvt_i32_f32_e32 v35, v35
	v_rndne_f32_e32 v36, v36
	v_rndne_f32_e32 v44, v44
	v_med3_f32 v37, v37, s36, v20
	v_med3_f32 v45, v45, s36, v20
	v_cvt_i32_f32_e32 v51, v51
	v_cvt_i32_f32_sdwa v59, v59 dst_sel:WORD_1 dst_unused:UNUSED_PAD src0_sel:DWORD
	v_rndne_f32_e32 v52, v52
	v_rndne_f32_e32 v60, v60
	v_med3_f32 v53, v53, s36, v20
	v_med3_f32 v61, v61, s36, v20
	v_cvt_i32_f32_e32 v71, v71
	v_rndne_f32_e32 v72, v72
	v_med3_f32 v73, v73, s36, v20
	v_cvt_i32_f32_e32 v87, v87
	v_rndne_f32_e32 v88, v88
	v_med3_f32 v89, v89, s36, v20
	v_cvt_i32_f32_e32 v40, v40
	v_rndne_f32_e32 v41, v41
	v_cvt_i32_f32_e32 v56, v56
	v_rndne_f32_e32 v57, v57
	v_cvt_i32_f32_sdwa v74, v74 dst_sel:BYTE_3 dst_unused:UNUSED_PAD src0_sel:DWORD
	v_rndne_f32_e32 v78, v78
	v_med3_f32 v79, v79, s36, v20
	v_mul_f32_e32 v81, v32, v81
	v_cvt_i32_f32_sdwa v29, v29 dst_sel:BYTE_3 dst_unused:UNUSED_PAD src0_sel:DWORD
	v_rndne_f32_e32 v30, v30
	v_med3_f32 v31, v31, s36, v20
	v_mul_f32_e32 v32, v32, v97
	v_cvt_i32_f32_sdwa v46, v46 dst_sel:BYTE_3 dst_unused:UNUSED_PAD src0_sel:DWORD
	v_rndne_f32_e32 v47, v47
	v_med3_f32 v49, v49, s36, v20
	v_cvt_i32_f32_sdwa v62, v62 dst_sel:BYTE_3 dst_unused:UNUSED_PAD src0_sel:DWORD
	v_rndne_f32_e32 v63, v63
	v_med3_f32 v65, v65, s36, v20
	v_cvt_i32_f32_e32 v67, v67
	v_cvt_i32_f32_sdwa v75, v75 dst_sel:WORD_1 dst_unused:UNUSED_PAD src0_sel:DWORD
	v_rndne_f32_e32 v68, v68
	v_rndne_f32_e32 v76, v76
	v_med3_f32 v69, v69, s36, v20
	v_med3_f32 v77, v77, s36, v20
	v_cvt_i32_f32_e32 v83, v83
	v_cvt_i32_f32_sdwa v90, v90 dst_sel:WORD_1 dst_unused:UNUSED_PAD src0_sel:DWORD
	v_rndne_f32_e32 v84, v84
	v_rndne_f32_e32 v91, v91
	v_med3_f32 v85, v85, s36, v20
	v_med3_f32 v92, v92, s36, v20
	v_cvt_i32_f32_e32 v36, v36
	v_cvt_i32_f32_sdwa v44, v44 dst_sel:WORD_1 dst_unused:UNUSED_PAD src0_sel:DWORD
	v_rndne_f32_e32 v37, v37
	v_rndne_f32_e32 v45, v45
	v_cvt_i32_f32_e32 v52, v52
	v_cvt_i32_f32_sdwa v60, v60 dst_sel:WORD_1 dst_unused:UNUSED_PAD src0_sel:DWORD
	v_rndne_f32_e32 v53, v53
	v_rndne_f32_e32 v61, v61
	v_cvt_i32_f32_e32 v72, v72
	v_rndne_f32_e32 v73, v73
	v_cvt_i32_f32_e32 v88, v88
	v_rndne_f32_e32 v89, v89
	v_cvt_i32_f32_e32 v41, v41
	v_cvt_i32_f32_e32 v57, v57
	v_cvt_i32_f32_sdwa v78, v78 dst_sel:BYTE_3 dst_unused:UNUSED_PAD src0_sel:DWORD
	v_rndne_f32_e32 v79, v79
	v_med3_f32 v81, v81, s36, v20
	v_cvt_i32_f32_sdwa v30, v30 dst_sel:BYTE_3 dst_unused:UNUSED_PAD src0_sel:DWORD
	v_rndne_f32_e32 v31, v31
	v_med3_f32 v32, v32, s36, v20
	v_cvt_i32_f32_sdwa v47, v47 dst_sel:BYTE_3 dst_unused:UNUSED_PAD src0_sel:DWORD
	v_rndne_f32_e32 v49, v49
	v_cvt_i32_f32_sdwa v63, v63 dst_sel:BYTE_3 dst_unused:UNUSED_PAD src0_sel:DWORD
	v_rndne_f32_e32 v65, v65
	v_cvt_i32_f32_e32 v68, v68
	v_cvt_i32_f32_sdwa v76, v76 dst_sel:WORD_1 dst_unused:UNUSED_PAD src0_sel:DWORD
	v_rndne_f32_e32 v69, v69
	v_rndne_f32_e32 v77, v77
	v_cvt_i32_f32_e32 v84, v84
	v_cvt_i32_f32_sdwa v91, v91 dst_sel:WORD_1 dst_unused:UNUSED_PAD src0_sel:DWORD
	v_rndne_f32_e32 v85, v85
	v_rndne_f32_e32 v92, v92
	v_cvt_i32_f32_e32 v37, v37
	v_cvt_i32_f32_sdwa v45, v45 dst_sel:WORD_1 dst_unused:UNUSED_PAD src0_sel:DWORD
	v_cvt_i32_f32_e32 v53, v53
	v_cvt_i32_f32_sdwa v61, v61 dst_sel:WORD_1 dst_unused:UNUSED_PAD src0_sel:DWORD
	v_cvt_i32_f32_e32 v73, v73
	v_cvt_i32_f32_e32 v89, v89
	v_lshlrev_b32_e32 v34, 8, v34
	v_lshlrev_b32_e32 v50, 8, v50
	v_cvt_i32_f32_sdwa v79, v79 dst_sel:BYTE_3 dst_unused:UNUSED_PAD src0_sel:DWORD
	v_rndne_f32_e32 v81, v81
	v_cvt_i32_f32_sdwa v31, v31 dst_sel:BYTE_3 dst_unused:UNUSED_PAD src0_sel:DWORD
	v_rndne_f32_e32 v32, v32
	v_cvt_i32_f32_sdwa v49, v49 dst_sel:BYTE_3 dst_unused:UNUSED_PAD src0_sel:DWORD
; __device__ __forceinline__ void cvt_item_i8(const float* src, int ld, int k0, int c0, unsigned char* dst, int Kd, int drow0, const float* cmx  , unsigned char* scr, int lane) {
;     ...
; #pragma unroll
;     for (int g = 0; g < 4; ++g)
; #pragma unroll
;         for (int i = 0; i < 4; ++i) *(unsigned*)(scr + (4 * c + i) * 132 + 32 * g + 4 * q) = pack_i8x4(v[g][0][i] * inv[i], v[g][1][i] * inv[i], v[g][2][i] * inv[i], v[g][3][i] * inv[i]);
;     asm volatile("s_waitcnt lgkmcnt(0)" ::: "memory");
; #pragma unroll
;     for (int r = 0; r < 4; ++r) { const int n = 8 * r + (lane >> 3), ch = lane & 7; const unsigned char* p = scr + n * 132 + ch * 16;
;         u32x4 o; o.x = *(const unsigned*)(p); o.y = *(const unsigned*)(p + 4); o.z = *(const unsigned*)(p + 8); o.w = *(const unsigned*)(p + 12);
;         *(u32x4*)(dst + (size_t)(drow0 + n) * Kd + k0 + 16 * ch) = o; }
;     asm volatile("s_waitcnt lgkmcnt(0)" ::: "memory");
;     ...
;     for (int it = first + F.gw; it < N; it += F.NGW) conv_item<GRP>(F, it);
	v_cvt_i32_f32_sdwa v65, v65 dst_sel:BYTE_3 dst_unused:UNUSED_PAD src0_sel:DWORD
	v_cvt_i32_f32_e32 v69, v69
	v_cvt_i32_f32_sdwa v77, v77 dst_sel:WORD_1 dst_unused:UNUSED_PAD src0_sel:DWORD
	v_cvt_i32_f32_e32 v85, v85
	v_cvt_i32_f32_sdwa v92, v92 dst_sel:WORD_1 dst_unused:UNUSED_PAD src0_sel:DWORD
	v_and_b32_e32 v38, 0xff0000, v38
	v_and_b32_e32 v54, 0xff0000, v54
	v_lshlrev_b32_e32 v66, 8, v66
	v_lshlrev_b32_e32 v82, 8, v82
	v_perm_b32 v33, v34, v33, s37
	v_lshlrev_b32_e32 v34, 8, v39
	v_and_b32_e32 v39, 0xff0000, v43
	v_perm_b32 v43, v50, v48, s37
	v_lshlrev_b32_e32 v48, 8, v55
	v_cvt_i32_f32_sdwa v81, v81 dst_sel:BYTE_3 dst_unused:UNUSED_PAD src0_sel:DWORD
	v_cvt_i32_f32_sdwa v32, v32 dst_sel:BYTE_3 dst_unused:UNUSED_PAD src0_sel:DWORD
	v_and_b32_e32 v70, 0xff0000, v70
	v_and_b32_e32 v86, 0xff0000, v86
	v_and_b32_e32 v50, 0xff0000, v59
	v_perm_b32 v55, v66, v64, s37
	v_lshlrev_b32_e32 v59, 8, v71
	v_perm_b32 v66, v82, v80, s37
	v_lshlrev_b32_e32 v71, 8, v87
	v_or3_b32 v33, v33, v38, v42
	v_perm_b32 v34, v34, v35, s37
	v_lshlrev_b32_e32 v35, 8, v40
	v_or3_b32 v40, v43, v54, v58
	v_perm_b32 v42, v48, v51, s37
	v_lshlrev_b32_e32 v43, 8, v56
	v_and_b32_e32 v64, 0xff0000, v75
	v_and_b32_e32 v75, 0xff0000, v90
	v_and_b32_e32 v38, 0xff0000, v44
	v_and_b32_e32 v44, 0xff0000, v60
	v_or3_b32 v48, v55, v70, v74
	v_perm_b32 v51, v59, v67, s37
	v_lshlrev_b32_e32 v54, 8, v72
	v_or3_b32 v29, v66, v86, v29
	v_perm_b32 v56, v71, v83, s37
	v_lshlrev_b32_e32 v58, 8, v88
	v_or3_b32 v34, v34, v39, v46
	v_perm_b32 v35, v35, v36, s37
	v_lshlrev_b32_e32 v36, 8, v41
	ds_write2_b32 v21, v33, v40 offset1:8
	v_or3_b32 v33, v42, v50, v62
	v_perm_b32 v40, v43, v52, s37
	v_lshlrev_b32_e32 v41, 8, v57
	v_and_b32_e32 v55, 0xff0000, v76
	v_and_b32_e32 v59, 0xff0000, v91
	v_and_b32_e32 v39, 0xff0000, v45
	v_and_b32_e32 v42, 0xff0000, v61
	v_or3_b32 v43, v51, v64, v78
	v_perm_b32 v45, v54, v68, s37
	v_lshlrev_b32_e32 v46, 8, v73
	ds_write2_b32 v21, v48, v29 offset0:16 offset1:24
	v_or3_b32 v29, v56, v75, v30
	v_perm_b32 v30, v58, v84, s37
	v_lshlrev_b32_e32 v48, 8, v89
	v_or3_b32 v35, v35, v38, v47
	v_perm_b32 v36, v36, v37, s37
	ds_write2_b32 v21, v34, v33 offset0:33 offset1:41
	v_or3_b32 v33, v40, v44, v63
	v_perm_b32 v34, v41, v53, s37
	v_and_b32_e32 v50, 0xff0000, v77
	v_and_b32_e32 v51, 0xff0000, v92
	v_or3_b32 v37, v45, v55, v79
	v_perm_b32 v38, v46, v69, s37
	ds_write2_b32 v21, v43, v29 offset0:49 offset1:57
	v_or3_b32 v29, v30, v59, v31
	v_perm_b32 v30, v48, v85, s37
	v_or3_b32 v31, v36, v39, v49
	ds_write2_b32 v21, v35, v33 offset0:66 offset1:74
	v_or3_b32 v33, v34, v42, v65
	v_or3_b32 v34, v38, v50, v81
	ds_write2_b32 v21, v37, v29 offset0:82 offset1:90
	v_or3_b32 v29, v30, v51, v32
	ds_write2_b32 v21, v31, v33 offset0:99 offset1:107
	ds_write2_b32 v21, v34, v29 offset0:115 offset1:123
	s_waitcnt lgkmcnt(0)
	ds_read2_b32 v[30:31], v22 offset1:1
	ds_read2_b32 v[32:33], v22 offset0:2 offset1:3
	ds_read2_b32 v[34:35], v23 offset1:1
	ds_read2_b32 v[36:37], v24 offset1:1
	ds_read2_b32 v[38:39], v25 offset1:1
	ds_read2_b32 v[40:41], v26 offset1:1
	ds_read2_b32 v[42:43], v27 offset1:1
	ds_read2_b32 v[44:45], v28 offset1:1
	s_waitcnt lgkmcnt(6)
	global_store_dwordx4 v[10:11], v[30:33], off
	s_waitcnt lgkmcnt(4)
	global_store_dwordx4 v[12:13], v[34:37], off
	s_waitcnt lgkmcnt(2)
	global_store_dwordx4 v[14:15], v[38:41], off
	s_waitcnt lgkmcnt(0)
	global_store_dwordx4 v[6:7], v[42:45], off
	s_waitcnt lgkmcnt(0)
	s_bitcmp0_b32 s100, 0
	s_cbranch_scc1 .Lcv3_exit
	s_waitcnt vmcnt(4)
	v_mov_b64_e32 v[6:7], v[128:129]
	v_mov_b64_e32 v[10:11], v[132:133]
	v_mov_b64_e32 v[12:13], v[134:135]
	v_mov_b64_e32 v[14:15], v[136:137]
	v_mov_b64_e32 v[30:31], v[120:121]
	v_mov_b64_e32 v[32:33], v[122:123]
	v_mov_b64_e32 v[34:35], v[144:145]
	v_mov_b64_e32 v[36:37], v[146:147]
	v_mov_b64_e32 v[38:39], v[148:149]
	v_mov_b64_e32 v[40:41], v[150:151]
	v_mov_b64_e32 v[42:43], v[152:153]
	v_mov_b64_e32 v[44:45], v[154:155]
	v_mov_b64_e32 v[46:47], v[156:157]
	v_mov_b64_e32 v[48:49], v[158:159]
	v_mov_b64_e32 v[50:51], v[160:161]
	v_mov_b64_e32 v[52:53], v[162:163]
	v_mov_b64_e32 v[54:55], v[164:165]
	v_mov_b64_e32 v[56:57], v[166:167]
	v_mov_b64_e32 v[58:59], v[168:169]
	v_mov_b64_e32 v[60:61], v[170:171]
	v_mov_b64_e32 v[62:63], v[172:173]
	v_mov_b64_e32 v[64:65], v[174:175]
	v_mov_b64_e32 v[66:67], v[176:177]
	v_mov_b64_e32 v[68:69], v[178:179]
	v_mov_b64_e32 v[70:71], v[180:181]
	v_mov_b64_e32 v[72:73], v[182:183]
	v_mov_b64_e32 v[74:75], v[184:185]
	v_mov_b64_e32 v[76:77], v[186:187]
	v_mov_b64_e32 v[78:79], v[188:189]
	v_mov_b64_e32 v[80:81], v[190:191]
	v_mov_b64_e32 v[82:83], v[210:211]
	v_mov_b64_e32 v[84:85], v[212:213]
	v_mov_b64_e32 v[86:87], v[214:215]
	v_mov_b64_e32 v[88:89], v[216:217]
	v_mov_b64_e32 v[90:91], v[218:219]
	v_mov_b64_e32 v[92:93], v[220:221]
	v_mov_b64_e32 v[94:95], v[222:223]
	v_mov_b64_e32 v[96:97], v[224:225]
	s_lshr_b32 s100, s100, 1
	s_branch .Lcv3_R
